# K-loop stage issue rebalanced in all four GEMMs (A-half-0 stage moved from phase 2 to phase 3, phase-2 wait vmcnt 6); plus arg-pointer lanes, in-proj first-trip peel
# speedup vs baseline: 1.0418x; 1.0048x over previous
_Z6mk_fwd4Args:
	s_mov_b64 s[52:53], s[0:1]
	s_load_dwordx2 s[0:1], s[0:1], 0xc0
	v_readfirstlane_b32 s61, v0
	s_mov_b32 s50, s2
	s_waitcnt lgkmcnt(0)
	s_mov_b64 s[100:101], s[0:1]
	v_writelane_b32 v254, s0, 0
	s_nop 1
	v_writelane_b32 v254, s1, 1
	s_load_dword s0, s[52:53], 0xd0
	v_mbcnt_lo_u32_b32 v0, -1, 0
	v_mbcnt_hi_u32_b32 v0, -1, v0
	s_waitcnt lgkmcnt(0)
	s_mov_b32 s99, s0
	s_load_dwordx4 s[4:7], s[52:53], 0x90
	s_load_dwordx4 s[8:11], s[52:53], 0xa0
	v_writelane_b32 v254, s0, 2
	s_waitcnt lgkmcnt(0)
	v_writelane_b32 v255, s4, 54
	v_writelane_b32 v255, s5, 55
	v_writelane_b32 v255, s6, 56
	v_writelane_b32 v255, s7, 57
	v_writelane_b32 v255, s8, 58
	v_writelane_b32 v255, s9, 59
	v_writelane_b32 v255, s10, 60
	v_writelane_b32 v255, s11, 61
	s_add_u32 s0, s52, 0xd0
	s_addc_u32 s1, s53, 0
	s_and_b32 s33, s61, 0xffffffc0
	v_writelane_b32 v254, s0, 3
	v_add_u32_e32 v0, s33, v0
	v_cmp_gt_i32_e32 vcc, 32, v0
	v_writelane_b32 v254, s1, 4
	s_and_saveexec_b64 s[0:1], vcc
	v_lshl_add_u32 v1, v0, 2, 0
	v_add_u32_e32 v1, 0x24a00, v1
	v_mov_b32_e32 v2, 0
	ds_write_b32 v1, v2
	s_or_b64 exec, exec, s[0:1]
	s_load_dwordx2 s[0:1], s[52:53], 0xc8
	s_waitcnt lgkmcnt(0)
	s_barrier
	v_cmp_eq_u32_e32 vcc, 0, v0
	v_writelane_b32 v254, s0, 5
	s_nop 1
	v_writelane_b32 v254, s1, 6
	s_load_dwordx2 s[0:1], s[52:53], 0xc0
	s_waitcnt lgkmcnt(0)
	s_add_u32 s0, s0, 0x4000
	s_addc_u32 s1, s1, 0
	v_writelane_b32 v254, s0, 7
	s_nop 1
	v_writelane_b32 v254, s1, 8
	s_getreg_b32 s0, hwreg(HW_REG_XCC_ID, 0, 4)
	s_and_b32 s0, s0, 15
	v_writelane_b32 v254, s0, 9
	s_and_saveexec_b64 s[0:1], vcc
	s_cbranch_execz .LBB0_6
	s_mov_b64 s[4:5], exec
	v_mbcnt_lo_u32_b32 v0, s4, 0
	v_mbcnt_hi_u32_b32 v0, s5, v0
	v_cmp_eq_u32_e32 vcc, 0, v0
	s_and_saveexec_b64 s[2:3], vcc
	s_cbranch_execz .LBB0_5
	v_readlane_b32 s6, v254, 9
	s_bcnt1_i32_b64 s4, s[4:5]
	s_lshl_b32 s6, s6, 8
	v_mov_b32_e32 v2, s4
	v_readlane_b32 s4, v254, 7
	v_mov_b32_e32 v1, s6
	v_readlane_b32 s5, v254, 8
	s_nop 4
	global_atomic_add v1, v1, v2, s[4:5] offset:1024 sc0

.LBB0_243:
	s_add_u32 s75, s6, 0x100
	s_addc_u32 s48, s7, 0
	s_lshl_b32 s49, s45, 8
	s_lshl_b32 s8, s45, 20
	s_bitset1_b32 s49, 7
	s_mov_b32 s80, -2
	s_mov_b64 s[6:7], 0
	s_cmp_eq_u32 s80, 28
	s_cselect_b64 s[34:35], -1, 0
	s_and_b64 s[24:25], s[0:1], s[34:35]
	s_andn2_b64 vcc, exec, s[24:25]
	v_mov_b32_e32 v128, v170
	v_mov_b32_e32 v129, v160
	s_add_u32 vcc_lo, s70, s6
	s_addc_u32 vcc_hi, s71, s7
	s_add_u32 s81, vcc_lo, 0x32000100
	s_addc_u32 s50, vcc_hi, 0
	s_and_b64 s[24:25], s[34:35], exec
	s_cselect_b32 s25, s73, s50
	s_cselect_b32 s24, s72, s81
	s_add_u32 s50, s75, s6
	s_addc_u32 s51, s48, s7
	s_and_b64 s[34:35], s[34:35], exec
	s_cselect_b32 s35, s79, s51
	s_cselect_b32 s34, s78, s50
	s_add_i32 s50, 0, 0x10000
	s_add_i32 s51, 0, 0x14000
	v_add_u32_e32 v142, s50, v177
	v_add_u32_e32 v158, s51, v177
	ds_read_b128 v[130:133], v142
	ds_read_b128 v[134:137], v142 offset:1024
	ds_read_b128 v[138:141], v142 offset:2048
	ds_read_b128 v[142:145], v142 offset:3072
	ds_read_b128 v[146:149], v158
	ds_read_b128 v[150:153], v158 offset:1024
	ds_read_b128 v[154:157], v158 offset:2048
	ds_read_b128 v[172:175], v158 offset:3072
	ds_read_b128 v[180:183], v178
	ds_read_b128 v[184:187], v178 offset:1024
	ds_read_b128 v[188:191], v178 offset:2048
	ds_read_b128 v[192:195], v178 offset:3072
	ds_read_b128 v[196:199], v178 offset:4096
	ds_read_b128 v[200:203], v178 offset:5120
	ds_read_b128 v[204:207], v178 offset:6144
	ds_read_b128 v[208:211], v178 offset:7168
	s_add_i32 m0, s97, 0xc000
	v_lshl_add_u64 v[158:159], vcc, 0, v[160:161]
	v_lshl_add_u64 v[158:159], v[158:159], 0, s[54:55]
	v_mov_b32_e32 v171, v161
	global_load_lds_dwordx4 v[158:159], off
	s_add_i32 m0, s97, 0xe000
	v_lshl_add_u64 v[158:159], vcc, 0, v[170:171]
	v_lshl_add_u64 v[158:159], v[158:159], 0, s[54:55]
	global_load_lds_dwordx4 v[158:159], off
	s_waitcnt vmcnt(8)
	s_waitcnt lgkmcnt(0)
	s_barrier
	s_setprio 1
	s_waitcnt lgkmcnt(0)
	v_mfma_f32_16x16x32_bf16 v[100:103], v[130:133], v[180:183], 0
	v_mfma_f32_16x16x32_bf16 v[96:99], v[138:141], v[180:183], 0
	v_mfma_f32_16x16x32_bf16 v[92:95], v[130:133], v[188:191], 0
	v_mfma_f32_16x16x32_bf16 v[88:91], v[138:141], v[188:191], 0
	v_mfma_f32_16x16x32_bf16 v[84:87], v[130:133], v[196:199], 0
	v_mfma_f32_16x16x32_bf16 v[80:83], v[138:141], v[196:199], 0
	v_mfma_f32_16x16x32_bf16 v[76:79], v[130:133], v[204:207], 0
	v_mfma_f32_16x16x32_bf16 v[72:75], v[138:141], v[204:207], 0
	v_mfma_f32_16x16x32_bf16 v[100:103], v[134:137], v[184:187], v[100:103]
	v_mfma_f32_16x16x32_bf16 v[96:99], v[142:145], v[184:187], v[96:99]
	v_mfma_f32_16x16x32_bf16 v[92:95], v[134:137], v[192:195], v[92:95]
	v_mfma_f32_16x16x32_bf16 v[88:91], v[142:145], v[192:195], v[88:91]
	v_mfma_f32_16x16x32_bf16 v[84:87], v[134:137], v[200:203], v[84:87]
	v_mfma_f32_16x16x32_bf16 v[80:83], v[142:145], v[200:203], v[80:83]
	v_mfma_f32_16x16x32_bf16 v[76:79], v[134:137], v[208:211], v[76:79]
	v_mfma_f32_16x16x32_bf16 v[72:75], v[142:145], v[208:211], v[72:75]
	s_setprio 0
	s_setprio 1
	v_mfma_f32_16x16x32_bf16 v[68:71], v[146:149], v[180:183], 0
	v_mfma_f32_16x16x32_bf16 v[64:67], v[154:157], v[180:183], 0
	v_mfma_f32_16x16x32_bf16 v[60:63], v[146:149], v[188:191], 0
	v_mfma_f32_16x16x32_bf16 v[56:59], v[154:157], v[188:191], 0
	v_mfma_f32_16x16x32_bf16 v[52:55], v[146:149], v[196:199], 0
	v_mfma_f32_16x16x32_bf16 v[48:51], v[154:157], v[196:199], 0
	v_mfma_f32_16x16x32_bf16 v[40:43], v[146:149], v[204:207], 0
	v_mfma_f32_16x16x32_bf16 v[32:35], v[154:157], v[204:207], 0
	v_mfma_f32_16x16x32_bf16 v[68:71], v[150:153], v[184:187], v[68:71]
	v_mfma_f32_16x16x32_bf16 v[64:67], v[172:175], v[184:187], v[64:67]
	v_mfma_f32_16x16x32_bf16 v[60:63], v[150:153], v[192:195], v[60:63]
	v_mfma_f32_16x16x32_bf16 v[56:59], v[172:175], v[192:195], v[56:59]
	v_mfma_f32_16x16x32_bf16 v[52:55], v[150:153], v[200:203], v[52:55]
	v_mfma_f32_16x16x32_bf16 v[48:51], v[172:175], v[200:203], v[48:51]
	v_mfma_f32_16x16x32_bf16 v[40:43], v[150:153], v[208:211], v[40:43]
	v_mfma_f32_16x16x32_bf16 v[32:35], v[172:175], v[208:211], v[32:35]
	s_setprio 0
	s_barrier
	s_add_i32 s50, s50, s61
	s_mov_b32 m0, s50
	ds_read_b128 v[180:183], v178 offset:16384
	ds_read_b128 v[184:187], v178 offset:17408
	ds_read_b128 v[188:191], v178 offset:18432
	ds_read_b128 v[192:195], v178 offset:19456
	ds_read_b128 v[196:199], v178 offset:20480
	ds_read_b128 v[200:203], v178 offset:21504
	ds_read_b128 v[204:207], v178 offset:22528
	ds_read_b128 v[208:211], v178 offset:23552
	s_nop 0
	global_load_lds_dwordx4 v168, s[34:35]
	s_add_i32 m0, s50, 0x2000
	s_add_u32 vcc_lo, s34, 0x8000
	s_addc_u32 vcc_hi, s35, 0
	s_add_i32 s50, s51, s61
	s_nop 0
	global_load_lds_dwordx4 v162, s[34:35]
	s_mov_b32 m0, s50
	s_nop 0
	global_load_lds_dwordx4 v168, vcc
	s_add_i32 m0, s50, 0x2000
	s_nop 0
	global_load_lds_dwordx4 v162, vcc
	s_waitcnt vmcnt(6)
	s_waitcnt lgkmcnt(0)
	s_barrier
	s_setprio 1
	s_waitcnt lgkmcnt(0)
	v_mfma_f32_16x16x32_bf16 v[44:47], v[130:133], v[180:183], 0
	v_mfma_f32_16x16x32_bf16 v[36:39], v[138:141], v[180:183], 0
	v_mfma_f32_16x16x32_bf16 v[28:31], v[130:133], v[188:191], 0
	v_mfma_f32_16x16x32_bf16 v[24:27], v[138:141], v[188:191], 0
	v_mfma_f32_16x16x32_bf16 v[20:23], v[130:133], v[196:199], 0
	v_mfma_f32_16x16x32_bf16 v[16:19], v[138:141], v[196:199], 0
	v_mfma_f32_16x16x32_bf16 v[12:15], v[130:133], v[204:207], 0
	v_mfma_f32_16x16x32_bf16 v[8:11], v[138:141], v[204:207], 0
	v_mfma_f32_16x16x32_bf16 v[44:47], v[134:137], v[184:187], v[44:47]
	v_mfma_f32_16x16x32_bf16 v[36:39], v[142:145], v[184:187], v[36:39]
	v_mfma_f32_16x16x32_bf16 v[28:31], v[134:137], v[192:195], v[28:31]
	v_mfma_f32_16x16x32_bf16 v[24:27], v[142:145], v[192:195], v[24:27]
	v_mfma_f32_16x16x32_bf16 v[20:23], v[134:137], v[200:203], v[20:23]
	v_mfma_f32_16x16x32_bf16 v[16:19], v[142:145], v[200:203], v[16:19]
	v_mfma_f32_16x16x32_bf16 v[12:15], v[134:137], v[208:211], v[12:15]
	v_mfma_f32_16x16x32_bf16 v[8:11], v[142:145], v[208:211], v[8:11]
	s_setprio 0
	s_setprio 1
	v_mfma_f32_16x16x32_bf16 v[4:7], v[146:149], v[180:183], 0
	v_mfma_f32_16x16x32_bf16 v[0:3], v[154:157], v[180:183], 0
	v_mfma_f32_16x16x32_bf16 v[104:107], v[146:149], v[188:191], 0
	v_mfma_f32_16x16x32_bf16 v[108:111], v[154:157], v[188:191], 0
	v_mfma_f32_16x16x32_bf16 v[112:115], v[146:149], v[196:199], 0
	v_mfma_f32_16x16x32_bf16 v[116:119], v[154:157], v[196:199], 0
	v_mfma_f32_16x16x32_bf16 v[120:123], v[146:149], v[204:207], 0
	v_mfma_f32_16x16x32_bf16 v[124:127], v[154:157], v[204:207], 0
	v_mfma_f32_16x16x32_bf16 v[4:7], v[150:153], v[184:187], v[4:7]
	v_mfma_f32_16x16x32_bf16 v[0:3], v[172:175], v[184:187], v[0:3]
	v_mfma_f32_16x16x32_bf16 v[104:107], v[150:153], v[192:195], v[104:107]
	v_mfma_f32_16x16x32_bf16 v[108:111], v[172:175], v[192:195], v[108:111]
	v_mfma_f32_16x16x32_bf16 v[112:115], v[150:153], v[200:203], v[112:115]
	v_mfma_f32_16x16x32_bf16 v[116:119], v[172:175], v[200:203], v[116:119]
	v_mfma_f32_16x16x32_bf16 v[120:123], v[150:153], v[208:211], v[120:123]
	v_mfma_f32_16x16x32_bf16 v[124:127], v[172:175], v[208:211], v[124:127]
	s_setprio 0
	s_barrier
	s_add_i32 s50, 0, 0x18000
	s_add_i32 s51, 0, 0x1c000
	v_add_u32_e32 v142, s50, v177
	v_add_u32_e32 v158, s51, v177
	ds_read_b128 v[130:133], v142
	ds_read_b128 v[134:137], v142 offset:1024
	ds_read_b128 v[138:141], v142 offset:2048
	ds_read_b128 v[142:145], v142 offset:3072
	ds_read_b128 v[146:149], v158
	ds_read_b128 v[150:153], v158 offset:1024
	ds_read_b128 v[154:157], v158 offset:2048
	ds_read_b128 v[172:175], v158 offset:3072
	s_mov_b32 m0, s29
	v_mov_b32_e32 v160, v129
	ds_read_b128 v[180:183], v178 offset:32768
	ds_read_b128 v[184:187], v178 offset:33792
	ds_read_b128 v[188:191], v178 offset:34816
	ds_read_b128 v[192:195], v178 offset:35840
	ds_read_b128 v[196:199], v178 offset:36864
	ds_read_b128 v[200:203], v178 offset:37888
	ds_read_b128 v[204:207], v178 offset:38912
	ds_read_b128 v[208:211], v178 offset:39936
	s_mov_b32 m0, s97
	s_nop 0
	global_load_lds_dwordx4 v164, s[24:25]
	s_mov_b32 m0, s28
	s_nop 0
	global_load_lds_dwordx4 v166, s[24:25]
	s_mov_b32 m0, s29
	v_mov_b32_e32 v170, v128
	global_load_lds_dwordx4 v160, s[24:25]
	s_mov_b32 m0, s30
	s_nop 0
	global_load_lds_dwordx4 v170, s[24:25]
	s_waitcnt vmcnt(8)
	s_waitcnt lgkmcnt(0)
	s_barrier
	s_setprio 1
	s_waitcnt lgkmcnt(0)
	v_mfma_f32_16x16x32_bf16 v[100:103], v[130:133], v[180:183], v[100:103]
	v_mfma_f32_16x16x32_bf16 v[96:99], v[138:141], v[180:183], v[96:99]
	v_mfma_f32_16x16x32_bf16 v[92:95], v[130:133], v[188:191], v[92:95]
	v_mfma_f32_16x16x32_bf16 v[88:91], v[138:141], v[188:191], v[88:91]
	v_mfma_f32_16x16x32_bf16 v[84:87], v[130:133], v[196:199], v[84:87]
	v_mfma_f32_16x16x32_bf16 v[80:83], v[138:141], v[196:199], v[80:83]
	v_mfma_f32_16x16x32_bf16 v[76:79], v[130:133], v[204:207], v[76:79]
	v_mfma_f32_16x16x32_bf16 v[72:75], v[138:141], v[204:207], v[72:75]
	v_mfma_f32_16x16x32_bf16 v[100:103], v[134:137], v[184:187], v[100:103]
	v_mfma_f32_16x16x32_bf16 v[96:99], v[142:145], v[184:187], v[96:99]
	v_mfma_f32_16x16x32_bf16 v[92:95], v[134:137], v[192:195], v[92:95]
	v_mfma_f32_16x16x32_bf16 v[88:91], v[142:145], v[192:195], v[88:91]
	v_mfma_f32_16x16x32_bf16 v[84:87], v[134:137], v[200:203], v[84:87]
	v_mfma_f32_16x16x32_bf16 v[80:83], v[142:145], v[200:203], v[80:83]
	v_mfma_f32_16x16x32_bf16 v[76:79], v[134:137], v[208:211], v[76:79]
	v_mfma_f32_16x16x32_bf16 v[72:75], v[142:145], v[208:211], v[72:75]
	s_setprio 0
	s_setprio 1
	v_mfma_f32_16x16x32_bf16 v[68:71], v[146:149], v[180:183], v[68:71]
	v_mfma_f32_16x16x32_bf16 v[64:67], v[154:157], v[180:183], v[64:67]
	v_mfma_f32_16x16x32_bf16 v[60:63], v[146:149], v[188:191], v[60:63]
	v_mfma_f32_16x16x32_bf16 v[56:59], v[154:157], v[188:191], v[56:59]
	v_mfma_f32_16x16x32_bf16 v[52:55], v[146:149], v[196:199], v[52:55]
	v_mfma_f32_16x16x32_bf16 v[48:51], v[154:157], v[196:199], v[48:51]
	v_mfma_f32_16x16x32_bf16 v[40:43], v[146:149], v[204:207], v[40:43]
	v_mfma_f32_16x16x32_bf16 v[32:35], v[154:157], v[204:207], v[32:35]
	v_mfma_f32_16x16x32_bf16 v[68:71], v[150:153], v[184:187], v[68:71]
	v_mfma_f32_16x16x32_bf16 v[64:67], v[172:175], v[184:187], v[64:67]
	v_mfma_f32_16x16x32_bf16 v[60:63], v[150:153], v[192:195], v[60:63]
	v_mfma_f32_16x16x32_bf16 v[56:59], v[172:175], v[192:195], v[56:59]
	v_mfma_f32_16x16x32_bf16 v[52:55], v[150:153], v[200:203], v[52:55]
	v_mfma_f32_16x16x32_bf16 v[48:51], v[172:175], v[200:203], v[48:51]
	v_mfma_f32_16x16x32_bf16 v[40:43], v[150:153], v[208:211], v[40:43]
	v_mfma_f32_16x16x32_bf16 v[32:35], v[172:175], v[208:211], v[32:35]
	s_setprio 0
	s_barrier
	v_mov_b32_e32 v169, v161
	ds_read_b128 v[180:183], v178 offset:49152
	ds_read_b128 v[184:187], v178 offset:50176
	ds_read_b128 v[188:191], v178 offset:51200
	ds_read_b128 v[192:195], v178 offset:52224
	ds_read_b128 v[196:199], v178 offset:53248
	ds_read_b128 v[200:203], v178 offset:54272
	ds_read_b128 v[204:207], v178 offset:55296
	ds_read_b128 v[208:211], v178 offset:56320
	s_add_i32 s50, s50, s61
	v_lshl_add_u64 v[128:129], s[34:35], 0, v[168:169]
	v_lshl_add_u64 v[128:129], v[128:129], 0, s[52:53]
	s_mov_b32 m0, s50
	v_mov_b32_e32 v163, v161
	global_load_lds_dwordx4 v[128:129], off
	s_add_i32 m0, s50, 0x2000
	v_mov_b32_e32 v165, v161
	v_lshl_add_u64 v[128:129], s[34:35], 0, v[162:163]
	s_add_u32 s34, s34, 0x8080
	v_lshl_add_u64 v[128:129], v[128:129], 0, s[52:53]
	s_addc_u32 s35, s35, 0
	s_add_i32 s50, s51, s61
	global_load_lds_dwordx4 v[128:129], off
	s_mov_b32 m0, s50
	v_mov_b32_e32 v167, v161
	global_load_lds_dwordx4 v168, s[34:35]
	s_add_i32 m0, s50, 0x2000
	s_nop 0
	global_load_lds_dwordx4 v162, s[34:35]
	s_mov_b32 m0, s31
	v_lshl_add_u64 v[128:129], s[24:25], 0, v[164:165]
	v_lshl_add_u64 v[128:129], v[128:129], 0, s[52:53]
	global_load_lds_dwordx4 v[128:129], off
	s_mov_b32 m0, s42
	v_lshl_add_u64 v[128:129], s[24:25], 0, v[166:167]
	v_lshl_add_u64 v[128:129], v[128:129], 0, s[52:53]
	global_load_lds_dwordx4 v[128:129], off
	s_waitcnt vmcnt(8)
	s_waitcnt lgkmcnt(0)
	s_barrier
	s_setprio 1
	s_waitcnt lgkmcnt(0)
	v_mfma_f32_16x16x32_bf16 v[44:47], v[130:133], v[180:183], v[44:47]
	v_mfma_f32_16x16x32_bf16 v[36:39], v[138:141], v[180:183], v[36:39]
	v_mfma_f32_16x16x32_bf16 v[28:31], v[130:133], v[188:191], v[28:31]
	v_mfma_f32_16x16x32_bf16 v[24:27], v[138:141], v[188:191], v[24:27]
	v_mfma_f32_16x16x32_bf16 v[20:23], v[130:133], v[196:199], v[20:23]
	v_mfma_f32_16x16x32_bf16 v[16:19], v[138:141], v[196:199], v[16:19]
	v_mfma_f32_16x16x32_bf16 v[12:15], v[130:133], v[204:207], v[12:15]
	v_mfma_f32_16x16x32_bf16 v[8:11], v[138:141], v[204:207], v[8:11]
	v_mfma_f32_16x16x32_bf16 v[44:47], v[134:137], v[184:187], v[44:47]
	v_mfma_f32_16x16x32_bf16 v[36:39], v[142:145], v[184:187], v[36:39]
	v_mfma_f32_16x16x32_bf16 v[28:31], v[134:137], v[192:195], v[28:31]
	v_mfma_f32_16x16x32_bf16 v[24:27], v[142:145], v[192:195], v[24:27]
	v_mfma_f32_16x16x32_bf16 v[20:23], v[134:137], v[200:203], v[20:23]
	v_mfma_f32_16x16x32_bf16 v[16:19], v[142:145], v[200:203], v[16:19]
	v_mfma_f32_16x16x32_bf16 v[12:15], v[134:137], v[208:211], v[12:15]
	v_mfma_f32_16x16x32_bf16 v[8:11], v[142:145], v[208:211], v[8:11]
	s_setprio 0
	s_setprio 1
	v_mfma_f32_16x16x32_bf16 v[4:7], v[146:149], v[180:183], v[4:7]
	v_mfma_f32_16x16x32_bf16 v[0:3], v[154:157], v[180:183], v[0:3]
	v_mfma_f32_16x16x32_bf16 v[104:107], v[146:149], v[188:191], v[104:107]
	v_mfma_f32_16x16x32_bf16 v[108:111], v[154:157], v[188:191], v[108:111]
	v_mfma_f32_16x16x32_bf16 v[112:115], v[146:149], v[196:199], v[112:115]
	v_mfma_f32_16x16x32_bf16 v[116:119], v[154:157], v[196:199], v[116:119]
	v_mfma_f32_16x16x32_bf16 v[120:123], v[146:149], v[204:207], v[120:123]
	v_mfma_f32_16x16x32_bf16 v[124:127], v[154:157], v[204:207], v[124:127]
	v_mfma_f32_16x16x32_bf16 v[4:7], v[150:153], v[184:187], v[4:7]
	v_mfma_f32_16x16x32_bf16 v[0:3], v[172:175], v[184:187], v[0:3]
	v_mfma_f32_16x16x32_bf16 v[104:107], v[150:153], v[192:195], v[104:107]
	v_mfma_f32_16x16x32_bf16 v[108:111], v[172:175], v[192:195], v[108:111]
	v_mfma_f32_16x16x32_bf16 v[112:115], v[150:153], v[200:203], v[112:115]
	v_mfma_f32_16x16x32_bf16 v[116:119], v[172:175], v[200:203], v[116:119]
	v_mfma_f32_16x16x32_bf16 v[120:123], v[150:153], v[208:211], v[120:123]
	v_mfma_f32_16x16x32_bf16 v[124:127], v[172:175], v[208:211], v[124:127]
	s_setprio 0
	s_barrier
	s_add_i32 s80, s80, 2
	s_add_u32 s6, s6, 0x100
	s_addc_u32 s7, s7, 0
	s_branch .LBB0_245
.LBB0_244:
	s_add_u32 vcc_lo, s70, s6
	s_addc_u32 vcc_hi, s71, s7
	s_add_u32 s81, vcc_lo, 0x32000100
	s_addc_u32 s50, vcc_hi, 0
	s_and_b64 s[24:25], s[34:35], exec
	s_cselect_b32 s25, s73, s50
	s_cselect_b32 s24, s72, s81
	s_add_u32 s50, s75, s6
	s_addc_u32 s51, s48, s7
	s_and_b64 s[34:35], s[34:35], exec
	s_cselect_b32 s35, s79, s51
	s_cselect_b32 s34, s78, s50
	s_add_i32 s50, 0, 0x10000
	s_add_i32 s51, 0, 0x14000
	v_add_u32_e32 v142, s50, v177
	v_add_u32_e32 v158, s51, v177
	ds_read_b128 v[130:133], v142
	ds_read_b128 v[134:137], v142 offset:1024
	ds_read_b128 v[138:141], v142 offset:2048
	ds_read_b128 v[142:145], v142 offset:3072
	ds_read_b128 v[146:149], v158
	ds_read_b128 v[150:153], v158 offset:1024
	ds_read_b128 v[154:157], v158 offset:2048
	ds_read_b128 v[172:175], v158 offset:3072
	ds_read_b128 v[180:183], v178
	ds_read_b128 v[184:187], v178 offset:1024
	ds_read_b128 v[188:191], v178 offset:2048
	ds_read_b128 v[192:195], v178 offset:3072
	ds_read_b128 v[196:199], v178 offset:4096
	ds_read_b128 v[200:203], v178 offset:5120
	ds_read_b128 v[204:207], v178 offset:6144
	ds_read_b128 v[208:211], v178 offset:7168
	s_add_i32 m0, s97, 0xc000
	v_lshl_add_u64 v[158:159], vcc, 0, v[160:161]
	v_lshl_add_u64 v[158:159], v[158:159], 0, s[54:55]
	v_mov_b32_e32 v171, v161
	global_load_lds_dwordx4 v[158:159], off
	s_add_i32 m0, s97, 0xe000
	v_lshl_add_u64 v[158:159], vcc, 0, v[170:171]
	v_lshl_add_u64 v[158:159], v[158:159], 0, s[54:55]
	global_load_lds_dwordx4 v[158:159], off
	s_waitcnt vmcnt(8)
	s_waitcnt lgkmcnt(0)
	s_barrier
	s_setprio 1
	s_waitcnt lgkmcnt(0)
	v_mfma_f32_16x16x32_bf16 v[100:103], v[130:133], v[180:183], v[100:103]
	v_mfma_f32_16x16x32_bf16 v[96:99], v[138:141], v[180:183], v[96:99]
	v_mfma_f32_16x16x32_bf16 v[92:95], v[130:133], v[188:191], v[92:95]
	v_mfma_f32_16x16x32_bf16 v[88:91], v[138:141], v[188:191], v[88:91]
	v_mfma_f32_16x16x32_bf16 v[84:87], v[130:133], v[196:199], v[84:87]
	v_mfma_f32_16x16x32_bf16 v[80:83], v[138:141], v[196:199], v[80:83]
	v_mfma_f32_16x16x32_bf16 v[76:79], v[130:133], v[204:207], v[76:79]
	v_mfma_f32_16x16x32_bf16 v[72:75], v[138:141], v[204:207], v[72:75]
	v_mfma_f32_16x16x32_bf16 v[100:103], v[134:137], v[184:187], v[100:103]
	v_mfma_f32_16x16x32_bf16 v[96:99], v[142:145], v[184:187], v[96:99]
	v_mfma_f32_16x16x32_bf16 v[92:95], v[134:137], v[192:195], v[92:95]
	v_mfma_f32_16x16x32_bf16 v[88:91], v[142:145], v[192:195], v[88:91]
	v_mfma_f32_16x16x32_bf16 v[84:87], v[134:137], v[200:203], v[84:87]
	v_mfma_f32_16x16x32_bf16 v[80:83], v[142:145], v[200:203], v[80:83]
	v_mfma_f32_16x16x32_bf16 v[76:79], v[134:137], v[208:211], v[76:79]
	v_mfma_f32_16x16x32_bf16 v[72:75], v[142:145], v[208:211], v[72:75]
	s_setprio 0
	s_setprio 1
	v_mfma_f32_16x16x32_bf16 v[68:71], v[146:149], v[180:183], v[68:71]
	v_mfma_f32_16x16x32_bf16 v[64:67], v[154:157], v[180:183], v[64:67]
	v_mfma_f32_16x16x32_bf16 v[60:63], v[146:149], v[188:191], v[60:63]
	v_mfma_f32_16x16x32_bf16 v[56:59], v[154:157], v[188:191], v[56:59]
	v_mfma_f32_16x16x32_bf16 v[52:55], v[146:149], v[196:199], v[52:55]
	v_mfma_f32_16x16x32_bf16 v[48:51], v[154:157], v[196:199], v[48:51]
	v_mfma_f32_16x16x32_bf16 v[40:43], v[146:149], v[204:207], v[40:43]
	v_mfma_f32_16x16x32_bf16 v[32:35], v[154:157], v[204:207], v[32:35]
	v_mfma_f32_16x16x32_bf16 v[68:71], v[150:153], v[184:187], v[68:71]
	v_mfma_f32_16x16x32_bf16 v[64:67], v[172:175], v[184:187], v[64:67]
	v_mfma_f32_16x16x32_bf16 v[60:63], v[150:153], v[192:195], v[60:63]
	v_mfma_f32_16x16x32_bf16 v[56:59], v[172:175], v[192:195], v[56:59]
	v_mfma_f32_16x16x32_bf16 v[52:55], v[150:153], v[200:203], v[52:55]
	v_mfma_f32_16x16x32_bf16 v[48:51], v[172:175], v[200:203], v[48:51]
	v_mfma_f32_16x16x32_bf16 v[40:43], v[150:153], v[208:211], v[40:43]
	v_mfma_f32_16x16x32_bf16 v[32:35], v[172:175], v[208:211], v[32:35]
	s_setprio 0
	s_barrier
	s_add_i32 s50, s50, s61
	s_mov_b32 m0, s50
	ds_read_b128 v[180:183], v178 offset:16384
	ds_read_b128 v[184:187], v178 offset:17408
	ds_read_b128 v[188:191], v178 offset:18432
	ds_read_b128 v[192:195], v178 offset:19456
	ds_read_b128 v[196:199], v178 offset:20480
	ds_read_b128 v[200:203], v178 offset:21504
	ds_read_b128 v[204:207], v178 offset:22528
	ds_read_b128 v[208:211], v178 offset:23552
	s_nop 0
	global_load_lds_dwordx4 v168, s[34:35]
	s_add_i32 m0, s50, 0x2000
	s_add_u32 vcc_lo, s34, 0x8000
	s_addc_u32 vcc_hi, s35, 0
	s_add_i32 s50, s51, s61
	s_nop 0
	global_load_lds_dwordx4 v162, s[34:35]
	s_mov_b32 m0, s50
	s_nop 0
	global_load_lds_dwordx4 v168, vcc
	s_add_i32 m0, s50, 0x2000
	s_nop 0
	global_load_lds_dwordx4 v162, vcc
	s_waitcnt vmcnt(6)
	s_waitcnt lgkmcnt(0)
	s_barrier
	s_setprio 1
	s_waitcnt lgkmcnt(0)
	v_mfma_f32_16x16x32_bf16 v[44:47], v[130:133], v[180:183], v[44:47]
	v_mfma_f32_16x16x32_bf16 v[36:39], v[138:141], v[180:183], v[36:39]
	v_mfma_f32_16x16x32_bf16 v[28:31], v[130:133], v[188:191], v[28:31]
	v_mfma_f32_16x16x32_bf16 v[24:27], v[138:141], v[188:191], v[24:27]
	v_mfma_f32_16x16x32_bf16 v[20:23], v[130:133], v[196:199], v[20:23]
	v_mfma_f32_16x16x32_bf16 v[16:19], v[138:141], v[196:199], v[16:19]
	v_mfma_f32_16x16x32_bf16 v[12:15], v[130:133], v[204:207], v[12:15]
	v_mfma_f32_16x16x32_bf16 v[8:11], v[138:141], v[204:207], v[8:11]
	v_mfma_f32_16x16x32_bf16 v[44:47], v[134:137], v[184:187], v[44:47]
	v_mfma_f32_16x16x32_bf16 v[36:39], v[142:145], v[184:187], v[36:39]
	v_mfma_f32_16x16x32_bf16 v[28:31], v[134:137], v[192:195], v[28:31]
	v_mfma_f32_16x16x32_bf16 v[24:27], v[142:145], v[192:195], v[24:27]
	v_mfma_f32_16x16x32_bf16 v[20:23], v[134:137], v[200:203], v[20:23]
	v_mfma_f32_16x16x32_bf16 v[16:19], v[142:145], v[200:203], v[16:19]
	v_mfma_f32_16x16x32_bf16 v[12:15], v[134:137], v[208:211], v[12:15]
	v_mfma_f32_16x16x32_bf16 v[8:11], v[142:145], v[208:211], v[8:11]
	s_setprio 0
	s_setprio 1
	v_mfma_f32_16x16x32_bf16 v[4:7], v[146:149], v[180:183], v[4:7]
	v_mfma_f32_16x16x32_bf16 v[0:3], v[154:157], v[180:183], v[0:3]
	v_mfma_f32_16x16x32_bf16 v[104:107], v[146:149], v[188:191], v[104:107]
	v_mfma_f32_16x16x32_bf16 v[108:111], v[154:157], v[188:191], v[108:111]
	v_mfma_f32_16x16x32_bf16 v[112:115], v[146:149], v[196:199], v[112:115]
	v_mfma_f32_16x16x32_bf16 v[116:119], v[154:157], v[196:199], v[116:119]
	v_mfma_f32_16x16x32_bf16 v[120:123], v[146:149], v[204:207], v[120:123]
	v_mfma_f32_16x16x32_bf16 v[124:127], v[154:157], v[204:207], v[124:127]
	v_mfma_f32_16x16x32_bf16 v[4:7], v[150:153], v[184:187], v[4:7]
	v_mfma_f32_16x16x32_bf16 v[0:3], v[172:175], v[184:187], v[0:3]
	v_mfma_f32_16x16x32_bf16 v[104:107], v[150:153], v[192:195], v[104:107]
	v_mfma_f32_16x16x32_bf16 v[108:111], v[172:175], v[192:195], v[108:111]
	v_mfma_f32_16x16x32_bf16 v[112:115], v[150:153], v[200:203], v[112:115]
	v_mfma_f32_16x16x32_bf16 v[116:119], v[172:175], v[200:203], v[116:119]
	v_mfma_f32_16x16x32_bf16 v[120:123], v[150:153], v[208:211], v[120:123]
	v_mfma_f32_16x16x32_bf16 v[124:127], v[172:175], v[208:211], v[124:127]
	s_setprio 0
	s_barrier
	s_add_i32 s50, 0, 0x18000
	s_add_i32 s51, 0, 0x1c000
	v_add_u32_e32 v142, s50, v177
	v_add_u32_e32 v158, s51, v177
	ds_read_b128 v[130:133], v142
	ds_read_b128 v[134:137], v142 offset:1024
	ds_read_b128 v[138:141], v142 offset:2048
	ds_read_b128 v[142:145], v142 offset:3072
	ds_read_b128 v[146:149], v158
	ds_read_b128 v[150:153], v158 offset:1024
	ds_read_b128 v[154:157], v158 offset:2048
	ds_read_b128 v[172:175], v158 offset:3072
	s_mov_b32 m0, s29
	v_mov_b32_e32 v160, v129
	ds_read_b128 v[180:183], v178 offset:32768
	ds_read_b128 v[184:187], v178 offset:33792
	ds_read_b128 v[188:191], v178 offset:34816
	ds_read_b128 v[192:195], v178 offset:35840
	ds_read_b128 v[196:199], v178 offset:36864
	ds_read_b128 v[200:203], v178 offset:37888
	ds_read_b128 v[204:207], v178 offset:38912
	ds_read_b128 v[208:211], v178 offset:39936
	s_mov_b32 m0, s97
	s_nop 0
	global_load_lds_dwordx4 v164, s[24:25]
	s_mov_b32 m0, s28
	s_nop 0
	global_load_lds_dwordx4 v166, s[24:25]
	s_mov_b32 m0, s29
	v_mov_b32_e32 v170, v128
	global_load_lds_dwordx4 v160, s[24:25]
	s_mov_b32 m0, s30
	s_nop 0
	global_load_lds_dwordx4 v170, s[24:25]
	s_waitcnt vmcnt(8)
	s_waitcnt lgkmcnt(0)
	s_barrier
	s_setprio 1
	s_waitcnt lgkmcnt(0)
	v_mfma_f32_16x16x32_bf16 v[100:103], v[130:133], v[180:183], v[100:103]
	v_mfma_f32_16x16x32_bf16 v[96:99], v[138:141], v[180:183], v[96:99]
	v_mfma_f32_16x16x32_bf16 v[92:95], v[130:133], v[188:191], v[92:95]
	v_mfma_f32_16x16x32_bf16 v[88:91], v[138:141], v[188:191], v[88:91]
	v_mfma_f32_16x16x32_bf16 v[84:87], v[130:133], v[196:199], v[84:87]
	v_mfma_f32_16x16x32_bf16 v[80:83], v[138:141], v[196:199], v[80:83]
	v_mfma_f32_16x16x32_bf16 v[76:79], v[130:133], v[204:207], v[76:79]
	v_mfma_f32_16x16x32_bf16 v[72:75], v[138:141], v[204:207], v[72:75]
	v_mfma_f32_16x16x32_bf16 v[100:103], v[134:137], v[184:187], v[100:103]
	v_mfma_f32_16x16x32_bf16 v[96:99], v[142:145], v[184:187], v[96:99]
	v_mfma_f32_16x16x32_bf16 v[92:95], v[134:137], v[192:195], v[92:95]
	v_mfma_f32_16x16x32_bf16 v[88:91], v[142:145], v[192:195], v[88:91]
	v_mfma_f32_16x16x32_bf16 v[84:87], v[134:137], v[200:203], v[84:87]
	v_mfma_f32_16x16x32_bf16 v[80:83], v[142:145], v[200:203], v[80:83]
	v_mfma_f32_16x16x32_bf16 v[76:79], v[134:137], v[208:211], v[76:79]
	v_mfma_f32_16x16x32_bf16 v[72:75], v[142:145], v[208:211], v[72:75]
	s_setprio 0
	s_setprio 1
	v_mfma_f32_16x16x32_bf16 v[68:71], v[146:149], v[180:183], v[68:71]
	v_mfma_f32_16x16x32_bf16 v[64:67], v[154:157], v[180:183], v[64:67]
	v_mfma_f32_16x16x32_bf16 v[60:63], v[146:149], v[188:191], v[60:63]
	v_mfma_f32_16x16x32_bf16 v[56:59], v[154:157], v[188:191], v[56:59]
	v_mfma_f32_16x16x32_bf16 v[52:55], v[146:149], v[196:199], v[52:55]
	v_mfma_f32_16x16x32_bf16 v[48:51], v[154:157], v[196:199], v[48:51]
	v_mfma_f32_16x16x32_bf16 v[40:43], v[146:149], v[204:207], v[40:43]
	v_mfma_f32_16x16x32_bf16 v[32:35], v[154:157], v[204:207], v[32:35]
	v_mfma_f32_16x16x32_bf16 v[68:71], v[150:153], v[184:187], v[68:71]
	v_mfma_f32_16x16x32_bf16 v[64:67], v[172:175], v[184:187], v[64:67]
	v_mfma_f32_16x16x32_bf16 v[60:63], v[150:153], v[192:195], v[60:63]
	v_mfma_f32_16x16x32_bf16 v[56:59], v[172:175], v[192:195], v[56:59]
	v_mfma_f32_16x16x32_bf16 v[52:55], v[150:153], v[200:203], v[52:55]
	v_mfma_f32_16x16x32_bf16 v[48:51], v[172:175], v[200:203], v[48:51]
	v_mfma_f32_16x16x32_bf16 v[40:43], v[150:153], v[208:211], v[40:43]
	v_mfma_f32_16x16x32_bf16 v[32:35], v[172:175], v[208:211], v[32:35]
	s_setprio 0
	s_barrier
	v_mov_b32_e32 v169, v161
	ds_read_b128 v[180:183], v178 offset:49152
	ds_read_b128 v[184:187], v178 offset:50176
	ds_read_b128 v[188:191], v178 offset:51200
	ds_read_b128 v[192:195], v178 offset:52224
	ds_read_b128 v[196:199], v178 offset:53248
	ds_read_b128 v[200:203], v178 offset:54272
	ds_read_b128 v[204:207], v178 offset:55296
	ds_read_b128 v[208:211], v178 offset:56320
	s_add_i32 s50, s50, s61
	v_lshl_add_u64 v[128:129], s[34:35], 0, v[168:169]
	v_lshl_add_u64 v[128:129], v[128:129], 0, s[52:53]
	s_mov_b32 m0, s50
	v_mov_b32_e32 v163, v161
	global_load_lds_dwordx4 v[128:129], off
	s_add_i32 m0, s50, 0x2000
	v_mov_b32_e32 v165, v161
	v_lshl_add_u64 v[128:129], s[34:35], 0, v[162:163]
	s_add_u32 s34, s34, 0x8080
	v_lshl_add_u64 v[128:129], v[128:129], 0, s[52:53]
	s_addc_u32 s35, s35, 0
	s_add_i32 s50, s51, s61
	global_load_lds_dwordx4 v[128:129], off
	s_mov_b32 m0, s50
	v_mov_b32_e32 v167, v161
	global_load_lds_dwordx4 v168, s[34:35]
	s_add_i32 m0, s50, 0x2000
	s_nop 0
	global_load_lds_dwordx4 v162, s[34:35]
	s_mov_b32 m0, s31
	v_lshl_add_u64 v[128:129], s[24:25], 0, v[164:165]
	v_lshl_add_u64 v[128:129], v[128:129], 0, s[52:53]
	global_load_lds_dwordx4 v[128:129], off
	s_mov_b32 m0, s42
	v_lshl_add_u64 v[128:129], s[24:25], 0, v[166:167]
	v_lshl_add_u64 v[128:129], v[128:129], 0, s[52:53]
	global_load_lds_dwordx4 v[128:129], off
	s_waitcnt vmcnt(8)
	s_waitcnt lgkmcnt(0)
	s_barrier
	s_setprio 1
	s_waitcnt lgkmcnt(0)
	v_mfma_f32_16x16x32_bf16 v[44:47], v[130:133], v[180:183], v[44:47]
	v_mfma_f32_16x16x32_bf16 v[36:39], v[138:141], v[180:183], v[36:39]
	v_mfma_f32_16x16x32_bf16 v[28:31], v[130:133], v[188:191], v[28:31]
	v_mfma_f32_16x16x32_bf16 v[24:27], v[138:141], v[188:191], v[24:27]
	v_mfma_f32_16x16x32_bf16 v[20:23], v[130:133], v[196:199], v[20:23]
	v_mfma_f32_16x16x32_bf16 v[16:19], v[138:141], v[196:199], v[16:19]
	v_mfma_f32_16x16x32_bf16 v[12:15], v[130:133], v[204:207], v[12:15]
	v_mfma_f32_16x16x32_bf16 v[8:11], v[138:141], v[204:207], v[8:11]
	v_mfma_f32_16x16x32_bf16 v[44:47], v[134:137], v[184:187], v[44:47]
	v_mfma_f32_16x16x32_bf16 v[36:39], v[142:145], v[184:187], v[36:39]
	v_mfma_f32_16x16x32_bf16 v[28:31], v[134:137], v[192:195], v[28:31]
	v_mfma_f32_16x16x32_bf16 v[24:27], v[142:145], v[192:195], v[24:27]
	v_mfma_f32_16x16x32_bf16 v[20:23], v[134:137], v[200:203], v[20:23]
	v_mfma_f32_16x16x32_bf16 v[16:19], v[142:145], v[200:203], v[16:19]
	v_mfma_f32_16x16x32_bf16 v[12:15], v[134:137], v[208:211], v[12:15]
	v_mfma_f32_16x16x32_bf16 v[8:11], v[142:145], v[208:211], v[8:11]
	s_setprio 0
	s_setprio 1
	v_mfma_f32_16x16x32_bf16 v[4:7], v[146:149], v[180:183], v[4:7]
	v_mfma_f32_16x16x32_bf16 v[0:3], v[154:157], v[180:183], v[0:3]
	v_mfma_f32_16x16x32_bf16 v[104:107], v[146:149], v[188:191], v[104:107]
	v_mfma_f32_16x16x32_bf16 v[108:111], v[154:157], v[188:191], v[108:111]
	v_mfma_f32_16x16x32_bf16 v[112:115], v[146:149], v[196:199], v[112:115]
	v_mfma_f32_16x16x32_bf16 v[116:119], v[154:157], v[196:199], v[116:119]
	v_mfma_f32_16x16x32_bf16 v[120:123], v[146:149], v[204:207], v[120:123]
	v_mfma_f32_16x16x32_bf16 v[124:127], v[154:157], v[204:207], v[124:127]
	v_mfma_f32_16x16x32_bf16 v[4:7], v[150:153], v[184:187], v[4:7]
	v_mfma_f32_16x16x32_bf16 v[0:3], v[172:175], v[184:187], v[0:3]
	v_mfma_f32_16x16x32_bf16 v[104:107], v[150:153], v[192:195], v[104:107]
	v_mfma_f32_16x16x32_bf16 v[108:111], v[172:175], v[192:195], v[108:111]
	v_mfma_f32_16x16x32_bf16 v[112:115], v[150:153], v[200:203], v[112:115]
	v_mfma_f32_16x16x32_bf16 v[116:119], v[172:175], v[200:203], v[116:119]
	v_mfma_f32_16x16x32_bf16 v[120:123], v[150:153], v[208:211], v[120:123]
	v_mfma_f32_16x16x32_bf16 v[124:127], v[172:175], v[208:211], v[124:127]
	s_setprio 0
	s_barrier
	s_add_i32 s80, s80, 2
	s_add_u32 s6, s6, 0x100
	s_addc_u32 s7, s7, 0
	s_cmp_gt_u32 s80, 29
	s_cbranch_scc1 .LBB0_247

.LBB0_247:
	s_min_i32 s0, s47, s88
	s_mul_i32 s0, s0, s41
	s_add_i32 s0, s0, s59
	s_min_i32 s24, s0, 0x2fff
	v_readlane_b32 s0, v254, 13
	v_readlane_b32 s1, v254, 14
	v_mbcnt_lo_u32_b32 v128, -1, 0
	v_mbcnt_hi_u32_b32 v128, -1, v128
	v_readlane_b32 s0, v255, 54
	v_readlane_b32 s1, v255, 55
	s_ashr_i32 s6, s24, 12
	s_add_i32 s80, s6, 21
	s_ashr_i32 s81, s80, 31
	s_lshl_b64 s[6:7], s[80:81], 25
	s_waitcnt lgkmcnt(0)
	s_add_u32 s0, s0, s6
	s_addc_u32 s1, s1, s7
	s_lshr_b32 s6, s24, 1
	s_and_b32 s8, s6, 0x7c0
	v_and_b32_e32 v129, 0xffff8, v128
	s_lshl_b32 s6, s24, 5
	v_lshlrev_b32_e32 v128, 2, v128
	v_add_lshl_u32 v129, v129, s8, 12
	s_and_b32 s6, s6, 0xfe0
	v_and_b32_e32 v128, 28, v128
	v_or3_b32 v128, v129, s6, v128
	v_mov_b32_e32 v129, v161
	v_lshl_add_u64 v[152:153], v[128:129], 2, s[0:1]
	v_add_co_u32_e32 v132, vcc, s90, v152
	s_nop 1
	v_addc_co_u32_e32 v133, vcc, 0, v153, vcc
	v_add_co_u32_e32 v136, vcc, s91, v152
	global_load_dwordx4 v[128:131], v[152:153], off nt
	s_nop 0
	global_load_dwordx4 v[132:135], v[132:133], off nt
	v_addc_co_u32_e32 v137, vcc, 0, v153, vcc
	v_add_co_u32_e32 v140, vcc, s92, v152
	s_nop 1
	v_addc_co_u32_e32 v141, vcc, 0, v153, vcc
	v_add_co_u32_e32 v144, vcc, s93, v152
	global_load_dwordx4 v[136:139], v[136:137], off nt
	s_nop 0
	global_load_dwordx4 v[140:143], v[140:141], off nt
	v_addc_co_u32_e32 v145, vcc, 0, v153, vcc
	v_add_co_u32_e32 v148, vcc, 0x14000, v152
	s_nop 1
	v_addc_co_u32_e32 v149, vcc, 0, v153, vcc
	v_add_co_u32_e32 v154, vcc, 0x18000, v152
	global_load_dwordx4 v[144:147], v[144:145], off nt
	s_nop 0
	global_load_dwordx4 v[148:151], v[148:149], off nt
	v_addc_co_u32_e32 v155, vcc, 0, v153, vcc
	v_add_co_u32_e32 v156, vcc, 0x1c000, v152
	s_nop 1
	v_addc_co_u32_e32 v157, vcc, 0, v153, vcc
	global_load_dwordx4 v[152:155], v[154:155], off nt
	s_nop 0
	global_load_dwordx4 v[156:159], v[156:157], off nt
	s_and_b64 vcc, exec, s[20:21]
	s_cbranch_vccz .LBB0_249
	s_barrier

.LBB0_284:
	s_mov_b32 s43, s45
	s_mov_b32 s83, s74
	s_andn2_b64 vcc, exec, s[76:77]
	s_cbranch_vccnz .LBB0_286
	s_branch .LBB0_287

.LBB0_637:
	s_add_u32 s64, s6, s36
	v_add_u32_e32 v142, s53, v175
	v_add_u32_e32 v154, s54, v175
	s_addc_u32 s65, s7, s37
	ds_read_b128 v[130:133], v142
	ds_read_b128 v[134:137], v142 offset:1024
	ds_read_b128 v[138:141], v142 offset:2048
	ds_read_b128 v[142:145], v142 offset:3072
	ds_read_b128 v[146:149], v154
	ds_read_b128 v[150:153], v154 offset:1024
	ds_read_b128 v[168:171], v154 offset:2048
	ds_read_b128 v[178:181], v154 offset:3072
	s_add_u32 s66, s64, 0x46000100
	s_addc_u32 s67, s65, 0
	s_and_b64 s[38:39], s[40:41], exec
	s_cselect_b32 s39, s13, s67
	s_cselect_b32 s38, s12, s66
	s_add_u32 s66, s27, s36
	s_addc_u32 s67, s59, s37
	s_and_b64 s[40:41], s[40:41], exec
	s_cselect_b32 s41, s31, s67
	s_cselect_b32 s40, s30, s66
	ds_read_b128 v[182:185], v176
	ds_read_b128 v[186:189], v176 offset:1024
	ds_read_b128 v[190:193], v176 offset:2048
	ds_read_b128 v[194:197], v176 offset:3072
	ds_read_b128 v[198:201], v176 offset:4096
	ds_read_b128 v[202:205], v176 offset:5120
	ds_read_b128 v[206:209], v176 offset:6144
	ds_read_b128 v[210:213], v176 offset:7168
	s_add_i32 m0, s11, 0xc000
	v_lshl_add_u64 v[154:155], s[64:65], 0, v[156:157]
	v_lshl_add_u64 v[154:155], v[154:155], 0, s[20:21]
	v_mov_b32_e32 v167, v157
	global_load_lds_dwordx4 v[154:155], off
	s_add_i32 m0, s11, 0xe000
	v_lshl_add_u64 v[154:155], s[64:65], 0, v[166:167]
	v_lshl_add_u64 v[154:155], v[154:155], 0, s[20:21]
	global_load_lds_dwordx4 v[154:155], off
	s_waitcnt vmcnt(8)
	s_waitcnt lgkmcnt(0)
	s_barrier
	s_setprio 1
	s_waitcnt lgkmcnt(0)
	v_mfma_f32_16x16x32_bf16 v[100:103], v[130:133], v[182:185], v[100:103]
	v_mfma_f32_16x16x32_bf16 v[96:99], v[138:141], v[182:185], v[96:99]
	v_mfma_f32_16x16x32_bf16 v[92:95], v[130:133], v[190:193], v[92:95]
	v_mfma_f32_16x16x32_bf16 v[88:91], v[138:141], v[190:193], v[88:91]
	v_mfma_f32_16x16x32_bf16 v[84:87], v[130:133], v[198:201], v[84:87]
	v_mfma_f32_16x16x32_bf16 v[76:79], v[138:141], v[198:201], v[76:79]
	v_mfma_f32_16x16x32_bf16 v[68:71], v[130:133], v[206:209], v[68:71]
	v_mfma_f32_16x16x32_bf16 v[60:63], v[138:141], v[206:209], v[60:63]
	v_mfma_f32_16x16x32_bf16 v[100:103], v[134:137], v[186:189], v[100:103]
	v_mfma_f32_16x16x32_bf16 v[96:99], v[142:145], v[186:189], v[96:99]
	v_mfma_f32_16x16x32_bf16 v[92:95], v[134:137], v[194:197], v[92:95]
	v_mfma_f32_16x16x32_bf16 v[88:91], v[142:145], v[194:197], v[88:91]
	v_mfma_f32_16x16x32_bf16 v[84:87], v[134:137], v[202:205], v[84:87]
	v_mfma_f32_16x16x32_bf16 v[76:79], v[142:145], v[202:205], v[76:79]
	v_mfma_f32_16x16x32_bf16 v[68:71], v[134:137], v[210:213], v[68:71]
	v_mfma_f32_16x16x32_bf16 v[60:63], v[142:145], v[210:213], v[60:63]
	s_setprio 0
	s_setprio 1
	v_mfma_f32_16x16x32_bf16 v[52:55], v[146:149], v[182:185], v[52:55]
	v_mfma_f32_16x16x32_bf16 v[44:47], v[168:171], v[182:185], v[44:47]
	v_mfma_f32_16x16x32_bf16 v[36:39], v[146:149], v[190:193], v[36:39]
	v_mfma_f32_16x16x32_bf16 v[28:31], v[168:171], v[190:193], v[28:31]
	v_mfma_f32_16x16x32_bf16 v[20:23], v[146:149], v[198:201], v[20:23]
	v_mfma_f32_16x16x32_bf16 v[12:15], v[168:171], v[198:201], v[12:15]
	v_mfma_f32_16x16x32_bf16 v[8:11], v[146:149], v[206:209], v[8:11]
	v_mfma_f32_16x16x32_bf16 v[4:7], v[168:171], v[206:209], v[4:7]
	v_mfma_f32_16x16x32_bf16 v[52:55], v[150:153], v[186:189], v[52:55]
	v_mfma_f32_16x16x32_bf16 v[44:47], v[178:181], v[186:189], v[44:47]
	v_mfma_f32_16x16x32_bf16 v[36:39], v[150:153], v[194:197], v[36:39]
	v_mfma_f32_16x16x32_bf16 v[28:31], v[178:181], v[194:197], v[28:31]
	v_mfma_f32_16x16x32_bf16 v[20:23], v[150:153], v[202:205], v[20:23]
	v_mfma_f32_16x16x32_bf16 v[12:15], v[178:181], v[202:205], v[12:15]
	v_mfma_f32_16x16x32_bf16 v[8:11], v[150:153], v[210:213], v[8:11]
	v_mfma_f32_16x16x32_bf16 v[4:7], v[178:181], v[210:213], v[4:7]
	s_setprio 0
	s_barrier
	s_add_i32 s64, s53, s42
	s_mov_b32 m0, s64
	ds_read_b128 v[182:185], v176 offset:16384
	ds_read_b128 v[186:189], v176 offset:17408
	ds_read_b128 v[190:193], v176 offset:18432
	ds_read_b128 v[194:197], v176 offset:19456
	ds_read_b128 v[198:201], v176 offset:20480
	ds_read_b128 v[202:205], v176 offset:21504
	ds_read_b128 v[206:209], v176 offset:22528
	ds_read_b128 v[210:213], v176 offset:23552
	s_nop 0
	global_load_lds_dwordx4 v164, s[40:41]
	s_add_i32 m0, s64, 0x2000
	s_add_u32 s64, s40, 0x8000
	s_addc_u32 s65, s41, 0
	s_add_i32 s66, s54, s42
	s_nop 0
	global_load_lds_dwordx4 v158, s[40:41]
	s_mov_b32 m0, s66
	s_nop 0
	global_load_lds_dwordx4 v164, s[64:65]
	s_add_i32 m0, s66, 0x2000
	s_nop 0
	global_load_lds_dwordx4 v158, s[64:65]
	s_waitcnt vmcnt(6)
	s_waitcnt lgkmcnt(0)
	s_barrier
	s_setprio 1
	s_waitcnt lgkmcnt(0)
	v_mfma_f32_16x16x32_bf16 v[80:83], v[130:133], v[182:185], v[80:83]
	v_mfma_f32_16x16x32_bf16 v[72:75], v[138:141], v[182:185], v[72:75]
	v_mfma_f32_16x16x32_bf16 v[64:67], v[130:133], v[190:193], v[64:67]
	v_mfma_f32_16x16x32_bf16 v[56:59], v[138:141], v[190:193], v[56:59]
	v_mfma_f32_16x16x32_bf16 v[48:51], v[130:133], v[198:201], v[48:51]
	v_mfma_f32_16x16x32_bf16 v[40:43], v[138:141], v[198:201], v[40:43]
	v_mfma_f32_16x16x32_bf16 v[32:35], v[130:133], v[206:209], v[32:35]
	v_mfma_f32_16x16x32_bf16 v[24:27], v[138:141], v[206:209], v[24:27]
	v_mfma_f32_16x16x32_bf16 v[80:83], v[134:137], v[186:189], v[80:83]
	v_mfma_f32_16x16x32_bf16 v[72:75], v[142:145], v[186:189], v[72:75]
	v_mfma_f32_16x16x32_bf16 v[64:67], v[134:137], v[194:197], v[64:67]
	v_mfma_f32_16x16x32_bf16 v[56:59], v[142:145], v[194:197], v[56:59]
	v_mfma_f32_16x16x32_bf16 v[48:51], v[134:137], v[202:205], v[48:51]
	v_mfma_f32_16x16x32_bf16 v[40:43], v[142:145], v[202:205], v[40:43]
	v_mfma_f32_16x16x32_bf16 v[32:35], v[134:137], v[210:213], v[32:35]
	v_mfma_f32_16x16x32_bf16 v[24:27], v[142:145], v[210:213], v[24:27]
	s_setprio 0
	s_setprio 1
	v_mfma_f32_16x16x32_bf16 v[16:19], v[146:149], v[182:185], v[16:19]
	v_mfma_f32_16x16x32_bf16 v[0:3], v[168:171], v[182:185], v[0:3]
	v_mfma_f32_16x16x32_bf16 v[104:107], v[146:149], v[190:193], v[104:107]
	v_mfma_f32_16x16x32_bf16 v[108:111], v[168:171], v[190:193], v[108:111]
	v_mfma_f32_16x16x32_bf16 v[112:115], v[146:149], v[198:201], v[112:115]
	v_mfma_f32_16x16x32_bf16 v[116:119], v[168:171], v[198:201], v[116:119]
	v_mfma_f32_16x16x32_bf16 v[120:123], v[146:149], v[206:209], v[120:123]
	v_mfma_f32_16x16x32_bf16 v[124:127], v[168:171], v[206:209], v[124:127]
	v_mfma_f32_16x16x32_bf16 v[16:19], v[150:153], v[186:189], v[16:19]
	v_mfma_f32_16x16x32_bf16 v[0:3], v[178:181], v[186:189], v[0:3]
	v_mfma_f32_16x16x32_bf16 v[104:107], v[150:153], v[194:197], v[104:107]
	v_mfma_f32_16x16x32_bf16 v[108:111], v[178:181], v[194:197], v[108:111]
	v_mfma_f32_16x16x32_bf16 v[112:115], v[150:153], v[202:205], v[112:115]
	v_mfma_f32_16x16x32_bf16 v[116:119], v[178:181], v[202:205], v[116:119]
	v_mfma_f32_16x16x32_bf16 v[120:123], v[150:153], v[210:213], v[120:123]
	v_mfma_f32_16x16x32_bf16 v[124:127], v[178:181], v[210:213], v[124:127]
	s_setprio 0
	s_barrier
	s_add_i32 s64, 0, 0x18000
	s_add_i32 s65, 0, 0x1c000
	v_add_u32_e32 v142, s64, v175
	v_add_u32_e32 v154, s65, v175
	ds_read_b128 v[130:133], v142
	ds_read_b128 v[134:137], v142 offset:1024
	ds_read_b128 v[138:141], v142 offset:2048
	ds_read_b128 v[142:145], v142 offset:3072
	ds_read_b128 v[146:149], v154
	ds_read_b128 v[150:153], v154 offset:1024
	ds_read_b128 v[168:171], v154 offset:2048
	ds_read_b128 v[178:181], v154 offset:3072
	s_mov_b32 m0, s45
	v_mov_b32_e32 v156, v129
	ds_read_b128 v[182:185], v176 offset:32768
	ds_read_b128 v[186:189], v176 offset:33792
	ds_read_b128 v[190:193], v176 offset:34816
	ds_read_b128 v[194:197], v176 offset:35840
	ds_read_b128 v[198:201], v176 offset:36864
	ds_read_b128 v[202:205], v176 offset:37888
	ds_read_b128 v[206:209], v176 offset:38912
	ds_read_b128 v[210:213], v176 offset:39936
	s_mov_b32 m0, s11
	s_nop 0
	global_load_lds_dwordx4 v160, s[38:39]
	s_mov_b32 m0, s44
	s_nop 0
	global_load_lds_dwordx4 v162, s[38:39]
	s_mov_b32 m0, s45
	v_mov_b32_e32 v166, v128
	global_load_lds_dwordx4 v156, s[38:39]
	s_mov_b32 m0, s46
	s_nop 0
	global_load_lds_dwordx4 v166, s[38:39]
	s_waitcnt vmcnt(8)
	s_waitcnt lgkmcnt(0)
	s_barrier
	s_setprio 1
	s_waitcnt lgkmcnt(0)
	v_mfma_f32_16x16x32_bf16 v[100:103], v[130:133], v[182:185], v[100:103]
	v_mfma_f32_16x16x32_bf16 v[96:99], v[138:141], v[182:185], v[96:99]
	v_mfma_f32_16x16x32_bf16 v[92:95], v[130:133], v[190:193], v[92:95]
	v_mfma_f32_16x16x32_bf16 v[88:91], v[138:141], v[190:193], v[88:91]
	v_mfma_f32_16x16x32_bf16 v[84:87], v[130:133], v[198:201], v[84:87]
	v_mfma_f32_16x16x32_bf16 v[76:79], v[138:141], v[198:201], v[76:79]
	v_mfma_f32_16x16x32_bf16 v[68:71], v[130:133], v[206:209], v[68:71]
	v_mfma_f32_16x16x32_bf16 v[60:63], v[138:141], v[206:209], v[60:63]
	v_mfma_f32_16x16x32_bf16 v[100:103], v[134:137], v[186:189], v[100:103]
	v_mfma_f32_16x16x32_bf16 v[96:99], v[142:145], v[186:189], v[96:99]
	v_mfma_f32_16x16x32_bf16 v[92:95], v[134:137], v[194:197], v[92:95]
	v_mfma_f32_16x16x32_bf16 v[88:91], v[142:145], v[194:197], v[88:91]
	v_mfma_f32_16x16x32_bf16 v[84:87], v[134:137], v[202:205], v[84:87]
	v_mfma_f32_16x16x32_bf16 v[76:79], v[142:145], v[202:205], v[76:79]
	v_mfma_f32_16x16x32_bf16 v[68:71], v[134:137], v[210:213], v[68:71]
	v_mfma_f32_16x16x32_bf16 v[60:63], v[142:145], v[210:213], v[60:63]
	s_setprio 0
	s_setprio 1
	v_mfma_f32_16x16x32_bf16 v[52:55], v[146:149], v[182:185], v[52:55]
	v_mfma_f32_16x16x32_bf16 v[44:47], v[168:171], v[182:185], v[44:47]
	v_mfma_f32_16x16x32_bf16 v[36:39], v[146:149], v[190:193], v[36:39]
	v_mfma_f32_16x16x32_bf16 v[28:31], v[168:171], v[190:193], v[28:31]
	v_mfma_f32_16x16x32_bf16 v[20:23], v[146:149], v[198:201], v[20:23]
	v_mfma_f32_16x16x32_bf16 v[12:15], v[168:171], v[198:201], v[12:15]
	v_mfma_f32_16x16x32_bf16 v[8:11], v[146:149], v[206:209], v[8:11]
	v_mfma_f32_16x16x32_bf16 v[4:7], v[168:171], v[206:209], v[4:7]
	v_mfma_f32_16x16x32_bf16 v[52:55], v[150:153], v[186:189], v[52:55]
	v_mfma_f32_16x16x32_bf16 v[44:47], v[178:181], v[186:189], v[44:47]
	v_mfma_f32_16x16x32_bf16 v[36:39], v[150:153], v[194:197], v[36:39]
	v_mfma_f32_16x16x32_bf16 v[28:31], v[178:181], v[194:197], v[28:31]
	v_mfma_f32_16x16x32_bf16 v[20:23], v[150:153], v[202:205], v[20:23]
	v_mfma_f32_16x16x32_bf16 v[12:15], v[178:181], v[202:205], v[12:15]
	v_mfma_f32_16x16x32_bf16 v[8:11], v[150:153], v[210:213], v[8:11]
	v_mfma_f32_16x16x32_bf16 v[4:7], v[178:181], v[210:213], v[4:7]
	s_setprio 0
	s_barrier
	v_mov_b32_e32 v165, v157
	ds_read_b128 v[182:185], v176 offset:49152
	ds_read_b128 v[186:189], v176 offset:50176
	ds_read_b128 v[190:193], v176 offset:51200
	ds_read_b128 v[194:197], v176 offset:52224
	ds_read_b128 v[198:201], v176 offset:53248
	ds_read_b128 v[202:205], v176 offset:54272
	ds_read_b128 v[206:209], v176 offset:55296
	ds_read_b128 v[210:213], v176 offset:56320
	s_add_i32 s64, s64, s42
	v_lshl_add_u64 v[128:129], s[40:41], 0, v[164:165]
	v_lshl_add_u64 v[128:129], v[128:129], 0, s[18:19]
	s_mov_b32 m0, s64
	v_mov_b32_e32 v159, v157
	global_load_lds_dwordx4 v[128:129], off
	s_add_i32 m0, s64, 0x2000
	v_mov_b32_e32 v161, v157
	v_lshl_add_u64 v[128:129], s[40:41], 0, v[158:159]
	s_add_u32 s40, s40, 0x8080
	v_lshl_add_u64 v[128:129], v[128:129], 0, s[18:19]
	s_addc_u32 s41, s41, 0
	s_add_i32 s64, s65, s42
	global_load_lds_dwordx4 v[128:129], off
	s_mov_b32 m0, s64
	v_mov_b32_e32 v163, v157
	global_load_lds_dwordx4 v164, s[40:41]
	s_add_i32 m0, s64, 0x2000
	s_nop 0
	global_load_lds_dwordx4 v158, s[40:41]
	s_mov_b32 m0, s49
	v_lshl_add_u64 v[128:129], s[38:39], 0, v[160:161]
	v_lshl_add_u64 v[128:129], v[128:129], 0, s[18:19]
	global_load_lds_dwordx4 v[128:129], off
	s_mov_b32 m0, s50
	v_lshl_add_u64 v[128:129], s[38:39], 0, v[162:163]
	v_lshl_add_u64 v[128:129], v[128:129], 0, s[18:19]
	global_load_lds_dwordx4 v[128:129], off
	s_waitcnt vmcnt(8)
	s_waitcnt lgkmcnt(0)
	s_barrier
	s_setprio 1
	s_waitcnt lgkmcnt(0)
	v_mfma_f32_16x16x32_bf16 v[80:83], v[130:133], v[182:185], v[80:83]
	v_mfma_f32_16x16x32_bf16 v[72:75], v[138:141], v[182:185], v[72:75]
	v_mfma_f32_16x16x32_bf16 v[64:67], v[130:133], v[190:193], v[64:67]
	v_mfma_f32_16x16x32_bf16 v[56:59], v[138:141], v[190:193], v[56:59]
	v_mfma_f32_16x16x32_bf16 v[48:51], v[130:133], v[198:201], v[48:51]
	v_mfma_f32_16x16x32_bf16 v[40:43], v[138:141], v[198:201], v[40:43]
	v_mfma_f32_16x16x32_bf16 v[32:35], v[130:133], v[206:209], v[32:35]
	v_mfma_f32_16x16x32_bf16 v[24:27], v[138:141], v[206:209], v[24:27]
	v_mfma_f32_16x16x32_bf16 v[80:83], v[134:137], v[186:189], v[80:83]
	v_mfma_f32_16x16x32_bf16 v[72:75], v[142:145], v[186:189], v[72:75]
	v_mfma_f32_16x16x32_bf16 v[64:67], v[134:137], v[194:197], v[64:67]
	v_mfma_f32_16x16x32_bf16 v[56:59], v[142:145], v[194:197], v[56:59]
	v_mfma_f32_16x16x32_bf16 v[48:51], v[134:137], v[202:205], v[48:51]
	v_mfma_f32_16x16x32_bf16 v[40:43], v[142:145], v[202:205], v[40:43]
	v_mfma_f32_16x16x32_bf16 v[32:35], v[134:137], v[210:213], v[32:35]
	v_mfma_f32_16x16x32_bf16 v[24:27], v[142:145], v[210:213], v[24:27]
	s_setprio 0
	s_setprio 1
	v_mfma_f32_16x16x32_bf16 v[16:19], v[146:149], v[182:185], v[16:19]
	v_mfma_f32_16x16x32_bf16 v[0:3], v[168:171], v[182:185], v[0:3]
	v_mfma_f32_16x16x32_bf16 v[104:107], v[146:149], v[190:193], v[104:107]
	v_mfma_f32_16x16x32_bf16 v[108:111], v[168:171], v[190:193], v[108:111]
	v_mfma_f32_16x16x32_bf16 v[112:115], v[146:149], v[198:201], v[112:115]
	v_mfma_f32_16x16x32_bf16 v[116:119], v[168:171], v[198:201], v[116:119]
	v_mfma_f32_16x16x32_bf16 v[120:123], v[146:149], v[206:209], v[120:123]
	v_mfma_f32_16x16x32_bf16 v[124:127], v[168:171], v[206:209], v[124:127]
	v_mfma_f32_16x16x32_bf16 v[16:19], v[150:153], v[186:189], v[16:19]
	v_mfma_f32_16x16x32_bf16 v[0:3], v[178:181], v[186:189], v[0:3]
	v_mfma_f32_16x16x32_bf16 v[104:107], v[150:153], v[194:197], v[104:107]
	v_mfma_f32_16x16x32_bf16 v[108:111], v[178:181], v[194:197], v[108:111]
	v_mfma_f32_16x16x32_bf16 v[112:115], v[150:153], v[202:205], v[112:115]
	v_mfma_f32_16x16x32_bf16 v[116:119], v[178:181], v[202:205], v[116:119]
	v_mfma_f32_16x16x32_bf16 v[120:123], v[150:153], v[210:213], v[120:123]
	v_mfma_f32_16x16x32_bf16 v[124:127], v[178:181], v[210:213], v[124:127]
	s_setprio 0
	s_barrier
	s_add_i32 s63, s63, 2
	s_add_u32 s36, s36, 0x100
	s_addc_u32 s37, s37, 0
	s_cmp_gt_u32 s63, 29
	s_cbranch_scc1 .LBB0_642

.LBB0_901:
	s_cmp_lt_i32 s74, 1
	s_cbranch_scc1 .LBB0_904
	v_readlane_b32 s38, v254, 13
	v_readlane_b32 s39, v254, 14
	s_andn2_b64 vcc, exec, s[8:9]
	v_mbcnt_lo_u32_b32 v128, -1, 0
	v_mbcnt_hi_u32_b32 v128, -1, v128
	s_cbranch_vccnz .LBB0_904
	v_readlane_b32 s38, v255, 56
	v_readlane_b32 s39, v255, 57
	s_bitcmp1_b32 s74, 0
	v_lshlrev_b32_e32 v129, 2, v128
	s_cselect_b32 m0, s66, 0x24c00
	s_ashr_i32 s7, s6, 31
	v_add_u32_e32 v130, 0x780, v129
	v_cmp_gt_i32_e32 vcc, 32, v128
	s_lshl_b64 s[40:41], s[6:7], 14
	s_waitcnt lgkmcnt(0)
	s_add_u32 s38, s38, s40
	v_cndmask_b32_e32 v128, v130, v129, vcc
	v_lshl_add_u32 v128, s4, 7, v128
	s_addc_u32 s39, s39, s41
	v_ashrrev_i32_e32 v129, 31, v128
	v_lshl_add_u64 v[128:129], v[128:129], 2, s[38:39]
	global_load_lds_dwordx4 v[128:129], off

.LBB0_910:
	s_add_u32 s25, s36, 0x100
	s_addc_u32 s27, s37, 0
	s_lshl_b32 s7, s55, 10
	s_add_i32 s7, s7, 0x24000
	s_mov_b32 s42, -2
	s_mov_b64 s[36:37], 0
	s_cmp_eq_u32 s42, 12
	s_cselect_b64 s[40:41], -1, 0
	s_and_b64 s[38:39], s[34:35], s[40:41]
	s_andn2_b64 vcc, exec, s[38:39]
	v_mov_b32_e32 v128, v186
	v_mov_b32_e32 v129, v176
	s_add_u32 s76, s10, s36
	v_add_u32_e32 v134, s67, v194
	v_add_u32_e32 v142, s67, v195
	v_add_u32_e32 v150, s68, v194
	v_add_u32_e32 v158, s68, v195
	s_addc_u32 s77, s11, s37
	ds_read_b128 v[130:133], v134
	ds_read_b128 v[138:141], v134 offset:2048
	ds_read_b128 v[134:137], v142
	ds_read_b128 v[142:145], v142 offset:2048
	ds_read_b128 v[146:149], v150
	ds_read_b128 v[154:157], v150 offset:2048
	ds_read_b128 v[150:153], v158
	ds_read_b128 v[158:161], v158 offset:2048
	s_add_u32 s43, s76, 0x36000100
	s_addc_u32 s75, s77, 0
	s_and_b64 s[38:39], s[40:41], exec
	s_cselect_b32 s39, s13, s75
	s_cselect_b32 s38, s12, s43
	s_add_u32 s43, s25, s36
	s_addc_u32 s75, s27, s37
	s_and_b64 s[40:41], s[40:41], exec
	s_cselect_b32 s41, s31, s75
	s_cselect_b32 s40, s30, s43
	ds_read_b128 v[162:165], v227
	ds_read_b128 v[232:235], v227 offset:2048
	ds_read_b128 v[166:169], v228
	ds_read_b128 v[236:239], v228 offset:2048
	ds_read_b128 v[240:243], v227 offset:4096
	ds_read_b128 v[196:199], v227 offset:6144
	ds_read_b128 v[244:247], v228 offset:4096
	ds_read_b128 v[200:203], v228 offset:6144
	s_add_i32 m0, s50, 0xc000
	v_lshl_add_u64 v[170:171], s[76:77], 0, v[176:177]
	v_lshl_add_u64 v[170:171], v[170:171], 0, s[16:17]
	v_mov_b32_e32 v187, v177
	global_load_lds_dwordx4 v[170:171], off
	s_add_i32 m0, s50, 0xe000
	v_lshl_add_u64 v[170:171], s[76:77], 0, v[186:187]
	v_lshl_add_u64 v[170:171], v[170:171], 0, s[16:17]
	global_load_lds_dwordx4 v[170:171], off
	s_waitcnt vmcnt(8)
	s_waitcnt lgkmcnt(0)
	s_barrier
	s_setprio 1
	s_waitcnt lgkmcnt(0)
	v_mfma_scale_f32_16x16x128_f8f6f4 v[100:103], v[130:137], v[162:169], 0, v229, v229 op_sel_hi:[0,0,0]
	v_mfma_scale_f32_16x16x128_f8f6f4 v[96:99], v[138:145], v[162:169], 0, v229, v229 op_sel_hi:[0,0,0]
	v_mfma_scale_f32_16x16x128_f8f6f4 v[92:95], v[130:137], v[232:239], 0, v229, v229 op_sel_hi:[0,0,0]
	v_mfma_scale_f32_16x16x128_f8f6f4 v[88:91], v[138:145], v[232:239], 0, v229, v229 op_sel_hi:[0,0,0]
	v_mfma_scale_f32_16x16x128_f8f6f4 v[84:87], v[130:137], v[240:247], 0, v229, v229 op_sel_hi:[0,0,0]
	v_mfma_scale_f32_16x16x128_f8f6f4 v[80:83], v[138:145], v[240:247], 0, v229, v229 op_sel_hi:[0,0,0]
	v_mfma_scale_f32_16x16x128_f8f6f4 v[170:173], v[130:137], v[196:203], 0, v229, v229 op_sel_hi:[0,0,0]
	v_mfma_scale_f32_16x16x128_f8f6f4 v[188:191], v[138:145], v[196:203], 0, v229, v229 op_sel_hi:[0,0,0]
	s_setprio 0
	s_setprio 1
	v_mfma_scale_f32_16x16x128_f8f6f4 v[40:43], v[146:153], v[196:203], 0, v229, v229 op_sel_hi:[0,0,0]
	v_mfma_scale_f32_16x16x128_f8f6f4 v[32:35], v[154:161], v[196:203], 0, v229, v229 op_sel_hi:[0,0,0]
	v_mfma_scale_f32_16x16x128_f8f6f4 v[248:251], v[146:153], v[162:169], 0, v229, v229 op_sel_hi:[0,0,0]
	v_mfma_scale_f32_16x16x128_f8f6f4 v[204:207], v[154:161], v[162:169], 0, v229, v229 op_sel_hi:[0,0,0]
	v_mfma_scale_f32_16x16x128_f8f6f4 v[208:211], v[146:153], v[232:239], 0, v229, v229 op_sel_hi:[0,0,0]
	v_mfma_scale_f32_16x16x128_f8f6f4 v[212:215], v[154:161], v[232:239], 0, v229, v229 op_sel_hi:[0,0,0]
	v_mfma_scale_f32_16x16x128_f8f6f4 v[216:219], v[146:153], v[240:247], 0, v229, v229 op_sel_hi:[0,0,0]
	v_mfma_scale_f32_16x16x128_f8f6f4 v[240:243], v[154:161], v[240:247], 0, v229, v229 op_sel_hi:[0,0,0]
	s_setprio 0
	s_barrier
	s_add_i32 s43, s67, s5
	s_mov_b32 m0, s43
	s_nop 2
	ds_read_b128 v[48:51], v227 offset:16384
	ds_read_b128 v[56:59], v227 offset:18432
	ds_read_b128 v[52:55], v228 offset:16384
	ds_read_b128 v[60:63], v228 offset:18432
	ds_read_b128 v[64:67], v227 offset:20480
	ds_read_b128 v[72:75], v227 offset:22528
	ds_read_b128 v[68:71], v228 offset:20480
	ds_read_b128 v[76:79], v228 offset:22528
	s_nop 0
	global_load_lds_dwordx4 v184, s[40:41]
	s_add_i32 m0, s43, 0x2000
	s_add_u32 s76, s40, 0x4000
	s_addc_u32 s77, s41, 0
	s_add_i32 s43, s68, s5
	s_nop 0
	global_load_lds_dwordx4 v178, s[40:41]
	s_mov_b32 m0, s43
	s_nop 0
	global_load_lds_dwordx4 v184, s[76:77]
	s_add_i32 m0, s43, 0x2000
	s_nop 0
	global_load_lds_dwordx4 v178, s[76:77]
	s_waitcnt vmcnt(6)
	s_waitcnt lgkmcnt(0)
	s_barrier
	s_setprio 1
	s_waitcnt lgkmcnt(0)
	v_mfma_scale_f32_16x16x128_f8f6f4 v[44:47], v[130:137], v[48:55], 0, v229, v229 op_sel_hi:[0,0,0]
	v_mfma_scale_f32_16x16x128_f8f6f4 v[36:39], v[138:145], v[48:55], 0, v229, v229 op_sel_hi:[0,0,0]
	v_mfma_scale_f32_16x16x128_f8f6f4 v[28:31], v[130:137], v[56:63], 0, v229, v229 op_sel_hi:[0,0,0]
	v_mfma_scale_f32_16x16x128_f8f6f4 v[24:27], v[138:145], v[56:63], 0, v229, v229 op_sel_hi:[0,0,0]
	v_mfma_scale_f32_16x16x128_f8f6f4 v[20:23], v[130:137], v[64:71], 0, v229, v229 op_sel_hi:[0,0,0]
	v_mfma_scale_f32_16x16x128_f8f6f4 v[16:19], v[138:145], v[64:71], 0, v229, v229 op_sel_hi:[0,0,0]
	v_mfma_scale_f32_16x16x128_f8f6f4 v[12:15], v[130:137], v[72:79], 0, v229, v229 op_sel_hi:[0,0,0]
	v_mfma_scale_f32_16x16x128_f8f6f4 v[8:11], v[138:145], v[72:79], 0, v229, v229 op_sel_hi:[0,0,0]
	s_setprio 0
	s_setprio 1
	v_mfma_scale_f32_16x16x128_f8f6f4 v[4:7], v[146:153], v[48:55], 0, v229, v229 op_sel_hi:[0,0,0]
	v_mfma_scale_f32_16x16x128_f8f6f4 v[0:3], v[154:161], v[48:55], 0, v229, v229 op_sel_hi:[0,0,0]
	v_mfma_scale_f32_16x16x128_f8f6f4 v[104:107], v[146:153], v[56:63], 0, v229, v229 op_sel_hi:[0,0,0]
	v_mfma_scale_f32_16x16x128_f8f6f4 v[108:111], v[154:161], v[56:63], 0, v229, v229 op_sel_hi:[0,0,0]
	v_mfma_scale_f32_16x16x128_f8f6f4 v[112:115], v[146:153], v[64:71], 0, v229, v229 op_sel_hi:[0,0,0]
	v_mfma_scale_f32_16x16x128_f8f6f4 v[116:119], v[154:161], v[64:71], 0, v229, v229 op_sel_hi:[0,0,0]
	v_mfma_scale_f32_16x16x128_f8f6f4 v[120:123], v[146:153], v[72:79], 0, v229, v229 op_sel_hi:[0,0,0]
	v_mfma_scale_f32_16x16x128_f8f6f4 v[124:127], v[154:161], v[72:79], 0, v229, v229 op_sel_hi:[0,0,0]
	s_setprio 0
	s_barrier
	s_add_i32 s43, 0, 0x18000
	v_add_u32_e32 v48, s43, v194
	s_add_i32 s75, 0, 0x1c000
	v_add_u32_e32 v49, s43, v195
	ds_read_b128 v[130:133], v48
	ds_read_b128 v[138:141], v48 offset:2048
	ds_read_b128 v[134:137], v49
	ds_read_b128 v[142:145], v49 offset:2048
	v_add_u32_e32 v48, s75, v194
	v_add_u32_e32 v49, s75, v195
	ds_read_b128 v[146:149], v48
	ds_read_b128 v[154:157], v48 offset:2048
	ds_read_b128 v[150:153], v49
	ds_read_b128 v[158:161], v49 offset:2048
	s_mov_b32 m0, s52
	v_mov_b32_e32 v176, v129
	ds_read_b128 v[48:51], v227 offset:32768
	ds_read_b128 v[162:165], v227 offset:34816
	ds_read_b128 v[52:55], v228 offset:32768
	ds_read_b128 v[166:169], v228 offset:34816
	ds_read_b128 v[196:199], v227 offset:36864
	ds_read_b128 v[232:235], v227 offset:38912
	ds_read_b128 v[200:203], v228 offset:36864
	ds_read_b128 v[236:239], v228 offset:38912
	s_mov_b32 m0, s50
	s_nop 0
	global_load_lds_dwordx4 v180, s[38:39]
	s_mov_b32 m0, s51
	s_nop 0
	global_load_lds_dwordx4 v182, s[38:39]
	s_mov_b32 m0, s52
	v_mov_b32_e32 v186, v128
	global_load_lds_dwordx4 v176, s[38:39]
	s_mov_b32 m0, s53
	s_nop 0
	global_load_lds_dwordx4 v186, s[38:39]
	s_waitcnt vmcnt(8)
	s_waitcnt lgkmcnt(0)
	s_barrier
	s_setprio 1
	s_waitcnt lgkmcnt(0)
	v_mfma_scale_f32_16x16x128_f8f6f4 v[100:103], v[130:137], v[48:55], v[100:103], v229, v229 op_sel_hi:[0,0,0]
	v_mfma_scale_f32_16x16x128_f8f6f4 v[96:99], v[138:145], v[48:55], v[96:99], v229, v229 op_sel_hi:[0,0,0]
	v_mfma_scale_f32_16x16x128_f8f6f4 v[92:95], v[130:137], v[162:169], v[92:95], v229, v229 op_sel_hi:[0,0,0]
	v_mfma_scale_f32_16x16x128_f8f6f4 v[88:91], v[138:145], v[162:169], v[88:91], v229, v229 op_sel_hi:[0,0,0]
	v_mfma_scale_f32_16x16x128_f8f6f4 v[84:87], v[130:137], v[196:203], v[84:87], v229, v229 op_sel_hi:[0,0,0]
	v_mfma_scale_f32_16x16x128_f8f6f4 v[80:83], v[138:145], v[196:203], v[80:83], v229, v229 op_sel_hi:[0,0,0]
	v_mfma_scale_f32_16x16x128_f8f6f4 v[76:79], v[130:137], v[232:239], v[170:173], v229, v229 op_sel_hi:[0,0,0]
	v_mfma_scale_f32_16x16x128_f8f6f4 v[72:75], v[138:145], v[232:239], v[188:191], v229, v229 op_sel_hi:[0,0,0]
	s_setprio 0
	s_setprio 1
	v_mfma_scale_f32_16x16x128_f8f6f4 v[68:71], v[146:153], v[48:55], v[248:251], v229, v229 op_sel_hi:[0,0,0]
	v_mfma_scale_f32_16x16x128_f8f6f4 v[64:67], v[154:161], v[48:55], v[204:207], v229, v229 op_sel_hi:[0,0,0]
	v_mfma_scale_f32_16x16x128_f8f6f4 v[60:63], v[146:153], v[162:169], v[208:211], v229, v229 op_sel_hi:[0,0,0]
	v_mfma_scale_f32_16x16x128_f8f6f4 v[56:59], v[154:161], v[162:169], v[212:215], v229, v229 op_sel_hi:[0,0,0]
	v_mfma_scale_f32_16x16x128_f8f6f4 v[52:55], v[146:153], v[196:203], v[216:219], v229, v229 op_sel_hi:[0,0,0]
	v_mfma_scale_f32_16x16x128_f8f6f4 v[48:51], v[154:161], v[196:203], v[240:243], v229, v229 op_sel_hi:[0,0,0]
	v_mfma_scale_f32_16x16x128_f8f6f4 v[40:43], v[146:153], v[232:239], v[40:43], v229, v229 op_sel_hi:[0,0,0]
	v_mfma_scale_f32_16x16x128_f8f6f4 v[32:35], v[154:161], v[232:239], v[32:35], v229, v229 op_sel_hi:[0,0,0]
	s_setprio 0
	s_barrier
	v_mov_b32_e32 v185, v177
	ds_read_b128 v[162:165], v227 offset:49152
	ds_read_b128 v[196:199], v227 offset:51200
	ds_read_b128 v[166:169], v228 offset:49152
	ds_read_b128 v[200:203], v228 offset:51200
	ds_read_b128 v[232:235], v227 offset:53248
	ds_read_b128 v[240:243], v227 offset:55296
	ds_read_b128 v[236:239], v228 offset:53248
	ds_read_b128 v[244:247], v228 offset:55296
	s_add_i32 s43, s43, s5
	v_lshl_add_u64 v[128:129], s[40:41], 0, v[184:185]
	v_lshl_add_u64 v[128:129], v[128:129], 0, s[14:15]
	s_mov_b32 m0, s43
	v_mov_b32_e32 v179, v177
	global_load_lds_dwordx4 v[128:129], off
	s_add_i32 m0, s43, 0x2000
	v_mov_b32_e32 v181, v177
	v_lshl_add_u64 v[128:129], s[40:41], 0, v[178:179]
	s_add_u32 s40, s40, 0x4080
	v_lshl_add_u64 v[128:129], v[128:129], 0, s[14:15]
	s_addc_u32 s41, s41, 0
	s_add_i32 s43, s75, s5
	global_load_lds_dwordx4 v[128:129], off
	s_mov_b32 m0, s43
	v_mov_b32_e32 v183, v177
	global_load_lds_dwordx4 v184, s[40:41]
	s_add_i32 m0, s43, 0x2000
	s_nop 0
	global_load_lds_dwordx4 v178, s[40:41]
	s_mov_b32 m0, s62
	v_lshl_add_u64 v[128:129], s[38:39], 0, v[180:181]
	v_lshl_add_u64 v[128:129], v[128:129], 0, s[14:15]
	global_load_lds_dwordx4 v[128:129], off
	s_mov_b32 m0, s63
	v_lshl_add_u64 v[128:129], s[38:39], 0, v[182:183]
	v_lshl_add_u64 v[128:129], v[128:129], 0, s[14:15]
	global_load_lds_dwordx4 v[128:129], off
	s_waitcnt vmcnt(8)
	s_waitcnt lgkmcnt(0)
	s_barrier
	s_setprio 1
	s_waitcnt lgkmcnt(0)
	v_mfma_scale_f32_16x16x128_f8f6f4 v[44:47], v[130:137], v[162:169], v[44:47], v229, v229 op_sel_hi:[0,0,0]
	v_mfma_scale_f32_16x16x128_f8f6f4 v[36:39], v[138:145], v[162:169], v[36:39], v229, v229 op_sel_hi:[0,0,0]
	v_mfma_scale_f32_16x16x128_f8f6f4 v[28:31], v[130:137], v[196:203], v[28:31], v229, v229 op_sel_hi:[0,0,0]
	v_mfma_scale_f32_16x16x128_f8f6f4 v[24:27], v[138:145], v[196:203], v[24:27], v229, v229 op_sel_hi:[0,0,0]
	v_mfma_scale_f32_16x16x128_f8f6f4 v[20:23], v[130:137], v[232:239], v[20:23], v229, v229 op_sel_hi:[0,0,0]
	v_mfma_scale_f32_16x16x128_f8f6f4 v[16:19], v[138:145], v[232:239], v[16:19], v229, v229 op_sel_hi:[0,0,0]
	v_mfma_scale_f32_16x16x128_f8f6f4 v[12:15], v[130:137], v[240:247], v[12:15], v229, v229 op_sel_hi:[0,0,0]
	v_mfma_scale_f32_16x16x128_f8f6f4 v[8:11], v[138:145], v[240:247], v[8:11], v229, v229 op_sel_hi:[0,0,0]
	s_setprio 0
	s_setprio 1
	v_mfma_scale_f32_16x16x128_f8f6f4 v[4:7], v[146:153], v[162:169], v[4:7], v229, v229 op_sel_hi:[0,0,0]
	v_mfma_scale_f32_16x16x128_f8f6f4 v[0:3], v[154:161], v[162:169], v[0:3], v229, v229 op_sel_hi:[0,0,0]
	v_mfma_scale_f32_16x16x128_f8f6f4 v[104:107], v[146:153], v[196:203], v[104:107], v229, v229 op_sel_hi:[0,0,0]
	v_mfma_scale_f32_16x16x128_f8f6f4 v[108:111], v[154:161], v[196:203], v[108:111], v229, v229 op_sel_hi:[0,0,0]
	v_mfma_scale_f32_16x16x128_f8f6f4 v[112:115], v[146:153], v[232:239], v[112:115], v229, v229 op_sel_hi:[0,0,0]
	v_mfma_scale_f32_16x16x128_f8f6f4 v[116:119], v[154:161], v[232:239], v[116:119], v229, v229 op_sel_hi:[0,0,0]
	v_mfma_scale_f32_16x16x128_f8f6f4 v[120:123], v[146:153], v[240:247], v[120:123], v229, v229 op_sel_hi:[0,0,0]
	v_mfma_scale_f32_16x16x128_f8f6f4 v[124:127], v[154:161], v[240:247], v[124:127], v229, v229 op_sel_hi:[0,0,0]
	s_setprio 0
	s_barrier
	s_add_i32 s42, s42, 2
	s_add_u32 s36, s36, 0x100
	s_addc_u32 s37, s37, 0
	s_branch .LBB0_912
.LBB0_911:
	s_add_u32 s76, s10, s36
	v_add_u32_e32 v134, s67, v194
	v_add_u32_e32 v142, s67, v195
	v_add_u32_e32 v150, s68, v194
	v_add_u32_e32 v158, s68, v195
	s_addc_u32 s77, s11, s37
	ds_read_b128 v[130:133], v134
	ds_read_b128 v[138:141], v134 offset:2048
	ds_read_b128 v[134:137], v142
	ds_read_b128 v[142:145], v142 offset:2048
	ds_read_b128 v[146:149], v150
	ds_read_b128 v[154:157], v150 offset:2048
	ds_read_b128 v[150:153], v158
	ds_read_b128 v[158:161], v158 offset:2048
	s_add_u32 s43, s76, 0x36000100
	s_addc_u32 s75, s77, 0
	s_and_b64 s[38:39], s[40:41], exec
	s_cselect_b32 s39, s13, s75
	s_cselect_b32 s38, s12, s43
	s_add_u32 s43, s25, s36
	s_addc_u32 s75, s27, s37
	s_and_b64 s[40:41], s[40:41], exec
	s_cselect_b32 s41, s31, s75
	s_cselect_b32 s40, s30, s43
	ds_read_b128 v[162:165], v227
	ds_read_b128 v[232:235], v227 offset:2048
	ds_read_b128 v[166:169], v228
	ds_read_b128 v[236:239], v228 offset:2048
	ds_read_b128 v[240:243], v227 offset:4096
	ds_read_b128 v[196:199], v227 offset:6144
	ds_read_b128 v[244:247], v228 offset:4096
	ds_read_b128 v[200:203], v228 offset:6144
	s_add_i32 m0, s50, 0xc000
	v_lshl_add_u64 v[170:171], s[76:77], 0, v[176:177]
	v_lshl_add_u64 v[170:171], v[170:171], 0, s[16:17]
	v_mov_b32_e32 v187, v177
	global_load_lds_dwordx4 v[170:171], off
	s_add_i32 m0, s50, 0xe000
	v_lshl_add_u64 v[170:171], s[76:77], 0, v[186:187]
	v_lshl_add_u64 v[170:171], v[170:171], 0, s[16:17]
	global_load_lds_dwordx4 v[170:171], off
	s_waitcnt vmcnt(8)
	s_waitcnt lgkmcnt(0)
	s_barrier
	s_setprio 1
	s_waitcnt lgkmcnt(0)
	v_mfma_scale_f32_16x16x128_f8f6f4 v[100:103], v[130:137], v[162:169], v[100:103], v229, v229 op_sel_hi:[0,0,0]
	v_mfma_scale_f32_16x16x128_f8f6f4 v[96:99], v[138:145], v[162:169], v[96:99], v229, v229 op_sel_hi:[0,0,0]
	v_mfma_scale_f32_16x16x128_f8f6f4 v[92:95], v[130:137], v[232:239], v[92:95], v229, v229 op_sel_hi:[0,0,0]
	v_mfma_scale_f32_16x16x128_f8f6f4 v[88:91], v[138:145], v[232:239], v[88:91], v229, v229 op_sel_hi:[0,0,0]
	v_mfma_scale_f32_16x16x128_f8f6f4 v[84:87], v[130:137], v[240:247], v[84:87], v229, v229 op_sel_hi:[0,0,0]
	v_mfma_scale_f32_16x16x128_f8f6f4 v[80:83], v[138:145], v[240:247], v[80:83], v229, v229 op_sel_hi:[0,0,0]
	v_mfma_scale_f32_16x16x128_f8f6f4 v[170:173], v[130:137], v[196:203], v[76:79], v229, v229 op_sel_hi:[0,0,0]
	v_mfma_scale_f32_16x16x128_f8f6f4 v[188:191], v[138:145], v[196:203], v[72:75], v229, v229 op_sel_hi:[0,0,0]
	s_setprio 0
	s_setprio 1
	v_mfma_scale_f32_16x16x128_f8f6f4 v[40:43], v[146:153], v[196:203], v[40:43], v229, v229 op_sel_hi:[0,0,0]
	v_mfma_scale_f32_16x16x128_f8f6f4 v[32:35], v[154:161], v[196:203], v[32:35], v229, v229 op_sel_hi:[0,0,0]
	v_mfma_scale_f32_16x16x128_f8f6f4 v[248:251], v[146:153], v[162:169], v[68:71], v229, v229 op_sel_hi:[0,0,0]
	v_mfma_scale_f32_16x16x128_f8f6f4 v[204:207], v[154:161], v[162:169], v[64:67], v229, v229 op_sel_hi:[0,0,0]
	v_mfma_scale_f32_16x16x128_f8f6f4 v[208:211], v[146:153], v[232:239], v[60:63], v229, v229 op_sel_hi:[0,0,0]
	v_mfma_scale_f32_16x16x128_f8f6f4 v[212:215], v[154:161], v[232:239], v[56:59], v229, v229 op_sel_hi:[0,0,0]
	v_mfma_scale_f32_16x16x128_f8f6f4 v[216:219], v[146:153], v[240:247], v[52:55], v229, v229 op_sel_hi:[0,0,0]
	v_mfma_scale_f32_16x16x128_f8f6f4 v[240:243], v[154:161], v[240:247], v[48:51], v229, v229 op_sel_hi:[0,0,0]
	s_setprio 0
	s_barrier
	s_add_i32 s43, s67, s5
	s_mov_b32 m0, s43
	s_nop 2
	ds_read_b128 v[48:51], v227 offset:16384
	ds_read_b128 v[56:59], v227 offset:18432
	ds_read_b128 v[52:55], v228 offset:16384
	ds_read_b128 v[60:63], v228 offset:18432
	ds_read_b128 v[64:67], v227 offset:20480
	ds_read_b128 v[72:75], v227 offset:22528
	ds_read_b128 v[68:71], v228 offset:20480
	ds_read_b128 v[76:79], v228 offset:22528
	s_nop 0
	global_load_lds_dwordx4 v184, s[40:41]
	s_add_i32 m0, s43, 0x2000
	s_add_u32 s76, s40, 0x4000
	s_addc_u32 s77, s41, 0
	s_add_i32 s43, s68, s5
	s_nop 0
	global_load_lds_dwordx4 v178, s[40:41]
	s_mov_b32 m0, s43
	s_nop 0
	global_load_lds_dwordx4 v184, s[76:77]
	s_add_i32 m0, s43, 0x2000
	s_nop 0
	global_load_lds_dwordx4 v178, s[76:77]
	s_waitcnt vmcnt(6)
	s_waitcnt lgkmcnt(0)
	s_barrier
	s_setprio 1
	s_waitcnt lgkmcnt(0)
	v_mfma_scale_f32_16x16x128_f8f6f4 v[44:47], v[130:137], v[48:55], v[44:47], v229, v229 op_sel_hi:[0,0,0]
	v_mfma_scale_f32_16x16x128_f8f6f4 v[36:39], v[138:145], v[48:55], v[36:39], v229, v229 op_sel_hi:[0,0,0]
	v_mfma_scale_f32_16x16x128_f8f6f4 v[28:31], v[130:137], v[56:63], v[28:31], v229, v229 op_sel_hi:[0,0,0]
	v_mfma_scale_f32_16x16x128_f8f6f4 v[24:27], v[138:145], v[56:63], v[24:27], v229, v229 op_sel_hi:[0,0,0]
	v_mfma_scale_f32_16x16x128_f8f6f4 v[20:23], v[130:137], v[64:71], v[20:23], v229, v229 op_sel_hi:[0,0,0]
	v_mfma_scale_f32_16x16x128_f8f6f4 v[16:19], v[138:145], v[64:71], v[16:19], v229, v229 op_sel_hi:[0,0,0]
	v_mfma_scale_f32_16x16x128_f8f6f4 v[12:15], v[130:137], v[72:79], v[12:15], v229, v229 op_sel_hi:[0,0,0]
	v_mfma_scale_f32_16x16x128_f8f6f4 v[8:11], v[138:145], v[72:79], v[8:11], v229, v229 op_sel_hi:[0,0,0]
	s_setprio 0
	s_setprio 1
	v_mfma_scale_f32_16x16x128_f8f6f4 v[4:7], v[146:153], v[48:55], v[4:7], v229, v229 op_sel_hi:[0,0,0]
	v_mfma_scale_f32_16x16x128_f8f6f4 v[0:3], v[154:161], v[48:55], v[0:3], v229, v229 op_sel_hi:[0,0,0]
	v_mfma_scale_f32_16x16x128_f8f6f4 v[104:107], v[146:153], v[56:63], v[104:107], v229, v229 op_sel_hi:[0,0,0]
	v_mfma_scale_f32_16x16x128_f8f6f4 v[108:111], v[154:161], v[56:63], v[108:111], v229, v229 op_sel_hi:[0,0,0]
	v_mfma_scale_f32_16x16x128_f8f6f4 v[112:115], v[146:153], v[64:71], v[112:115], v229, v229 op_sel_hi:[0,0,0]
	v_mfma_scale_f32_16x16x128_f8f6f4 v[116:119], v[154:161], v[64:71], v[116:119], v229, v229 op_sel_hi:[0,0,0]
	v_mfma_scale_f32_16x16x128_f8f6f4 v[120:123], v[146:153], v[72:79], v[120:123], v229, v229 op_sel_hi:[0,0,0]
	v_mfma_scale_f32_16x16x128_f8f6f4 v[124:127], v[154:161], v[72:79], v[124:127], v229, v229 op_sel_hi:[0,0,0]
	s_setprio 0
	s_barrier
	s_add_i32 s43, 0, 0x18000
	v_add_u32_e32 v48, s43, v194
	s_add_i32 s75, 0, 0x1c000
	v_add_u32_e32 v49, s43, v195
	ds_read_b128 v[130:133], v48
	ds_read_b128 v[138:141], v48 offset:2048
	ds_read_b128 v[134:137], v49
	ds_read_b128 v[142:145], v49 offset:2048
	v_add_u32_e32 v48, s75, v194
	v_add_u32_e32 v49, s75, v195
	ds_read_b128 v[146:149], v48
	ds_read_b128 v[154:157], v48 offset:2048
	ds_read_b128 v[150:153], v49
	ds_read_b128 v[158:161], v49 offset:2048
	s_mov_b32 m0, s52
	v_mov_b32_e32 v176, v129
	ds_read_b128 v[48:51], v227 offset:32768
	ds_read_b128 v[162:165], v227 offset:34816
	ds_read_b128 v[52:55], v228 offset:32768
	ds_read_b128 v[166:169], v228 offset:34816
	ds_read_b128 v[196:199], v227 offset:36864
	ds_read_b128 v[232:235], v227 offset:38912
	ds_read_b128 v[200:203], v228 offset:36864
	ds_read_b128 v[236:239], v228 offset:38912
	s_mov_b32 m0, s50
	s_nop 0
	global_load_lds_dwordx4 v180, s[38:39]
	s_mov_b32 m0, s51
	s_nop 0
	global_load_lds_dwordx4 v182, s[38:39]
	s_mov_b32 m0, s52
	v_mov_b32_e32 v186, v128
	global_load_lds_dwordx4 v176, s[38:39]
	s_mov_b32 m0, s53
	s_nop 0
	global_load_lds_dwordx4 v186, s[38:39]
	s_waitcnt vmcnt(8)
	s_waitcnt lgkmcnt(0)
	s_barrier
	s_setprio 1
	s_waitcnt lgkmcnt(0)
	v_mfma_scale_f32_16x16x128_f8f6f4 v[100:103], v[130:137], v[48:55], v[100:103], v229, v229 op_sel_hi:[0,0,0]
	v_mfma_scale_f32_16x16x128_f8f6f4 v[96:99], v[138:145], v[48:55], v[96:99], v229, v229 op_sel_hi:[0,0,0]
	v_mfma_scale_f32_16x16x128_f8f6f4 v[92:95], v[130:137], v[162:169], v[92:95], v229, v229 op_sel_hi:[0,0,0]
	v_mfma_scale_f32_16x16x128_f8f6f4 v[88:91], v[138:145], v[162:169], v[88:91], v229, v229 op_sel_hi:[0,0,0]
	v_mfma_scale_f32_16x16x128_f8f6f4 v[84:87], v[130:137], v[196:203], v[84:87], v229, v229 op_sel_hi:[0,0,0]
	v_mfma_scale_f32_16x16x128_f8f6f4 v[80:83], v[138:145], v[196:203], v[80:83], v229, v229 op_sel_hi:[0,0,0]
	v_mfma_scale_f32_16x16x128_f8f6f4 v[76:79], v[130:137], v[232:239], v[170:173], v229, v229 op_sel_hi:[0,0,0]
	v_mfma_scale_f32_16x16x128_f8f6f4 v[72:75], v[138:145], v[232:239], v[188:191], v229, v229 op_sel_hi:[0,0,0]
	s_setprio 0
	s_setprio 1
	v_mfma_scale_f32_16x16x128_f8f6f4 v[68:71], v[146:153], v[48:55], v[248:251], v229, v229 op_sel_hi:[0,0,0]
	v_mfma_scale_f32_16x16x128_f8f6f4 v[64:67], v[154:161], v[48:55], v[204:207], v229, v229 op_sel_hi:[0,0,0]
	v_mfma_scale_f32_16x16x128_f8f6f4 v[60:63], v[146:153], v[162:169], v[208:211], v229, v229 op_sel_hi:[0,0,0]
	v_mfma_scale_f32_16x16x128_f8f6f4 v[56:59], v[154:161], v[162:169], v[212:215], v229, v229 op_sel_hi:[0,0,0]
	v_mfma_scale_f32_16x16x128_f8f6f4 v[52:55], v[146:153], v[196:203], v[216:219], v229, v229 op_sel_hi:[0,0,0]
	v_mfma_scale_f32_16x16x128_f8f6f4 v[48:51], v[154:161], v[196:203], v[240:243], v229, v229 op_sel_hi:[0,0,0]
	v_mfma_scale_f32_16x16x128_f8f6f4 v[40:43], v[146:153], v[232:239], v[40:43], v229, v229 op_sel_hi:[0,0,0]
	v_mfma_scale_f32_16x16x128_f8f6f4 v[32:35], v[154:161], v[232:239], v[32:35], v229, v229 op_sel_hi:[0,0,0]
	s_setprio 0
	s_barrier
	v_mov_b32_e32 v185, v177
	ds_read_b128 v[162:165], v227 offset:49152
	ds_read_b128 v[196:199], v227 offset:51200
	ds_read_b128 v[166:169], v228 offset:49152
	ds_read_b128 v[200:203], v228 offset:51200
	ds_read_b128 v[232:235], v227 offset:53248
	ds_read_b128 v[240:243], v227 offset:55296
	ds_read_b128 v[236:239], v228 offset:53248
	ds_read_b128 v[244:247], v228 offset:55296
	s_add_i32 s43, s43, s5
	v_lshl_add_u64 v[128:129], s[40:41], 0, v[184:185]
	v_lshl_add_u64 v[128:129], v[128:129], 0, s[14:15]
	s_mov_b32 m0, s43
	v_mov_b32_e32 v179, v177
	global_load_lds_dwordx4 v[128:129], off
	s_add_i32 m0, s43, 0x2000
	v_mov_b32_e32 v181, v177
	v_lshl_add_u64 v[128:129], s[40:41], 0, v[178:179]
	s_add_u32 s40, s40, 0x4080
	v_lshl_add_u64 v[128:129], v[128:129], 0, s[14:15]
	s_addc_u32 s41, s41, 0
	s_add_i32 s43, s75, s5
	global_load_lds_dwordx4 v[128:129], off
	s_mov_b32 m0, s43
	v_mov_b32_e32 v183, v177
	global_load_lds_dwordx4 v184, s[40:41]
	s_add_i32 m0, s43, 0x2000
	s_nop 0
	global_load_lds_dwordx4 v178, s[40:41]
	s_mov_b32 m0, s62
	v_lshl_add_u64 v[128:129], s[38:39], 0, v[180:181]
	v_lshl_add_u64 v[128:129], v[128:129], 0, s[14:15]
	global_load_lds_dwordx4 v[128:129], off
	s_mov_b32 m0, s63
	v_lshl_add_u64 v[128:129], s[38:39], 0, v[182:183]
	v_lshl_add_u64 v[128:129], v[128:129], 0, s[14:15]
	global_load_lds_dwordx4 v[128:129], off
	s_waitcnt vmcnt(8)
	s_waitcnt lgkmcnt(0)
	s_barrier
	s_setprio 1
	s_waitcnt lgkmcnt(0)
	v_mfma_scale_f32_16x16x128_f8f6f4 v[44:47], v[130:137], v[162:169], v[44:47], v229, v229 op_sel_hi:[0,0,0]
	v_mfma_scale_f32_16x16x128_f8f6f4 v[36:39], v[138:145], v[162:169], v[36:39], v229, v229 op_sel_hi:[0,0,0]
	v_mfma_scale_f32_16x16x128_f8f6f4 v[28:31], v[130:137], v[196:203], v[28:31], v229, v229 op_sel_hi:[0,0,0]
	v_mfma_scale_f32_16x16x128_f8f6f4 v[24:27], v[138:145], v[196:203], v[24:27], v229, v229 op_sel_hi:[0,0,0]
	v_mfma_scale_f32_16x16x128_f8f6f4 v[20:23], v[130:137], v[232:239], v[20:23], v229, v229 op_sel_hi:[0,0,0]
	v_mfma_scale_f32_16x16x128_f8f6f4 v[16:19], v[138:145], v[232:239], v[16:19], v229, v229 op_sel_hi:[0,0,0]
	v_mfma_scale_f32_16x16x128_f8f6f4 v[12:15], v[130:137], v[240:247], v[12:15], v229, v229 op_sel_hi:[0,0,0]
	v_mfma_scale_f32_16x16x128_f8f6f4 v[8:11], v[138:145], v[240:247], v[8:11], v229, v229 op_sel_hi:[0,0,0]
	s_setprio 0
	s_setprio 1
	v_mfma_scale_f32_16x16x128_f8f6f4 v[4:7], v[146:153], v[162:169], v[4:7], v229, v229 op_sel_hi:[0,0,0]
	v_mfma_scale_f32_16x16x128_f8f6f4 v[0:3], v[154:161], v[162:169], v[0:3], v229, v229 op_sel_hi:[0,0,0]
	v_mfma_scale_f32_16x16x128_f8f6f4 v[104:107], v[146:153], v[196:203], v[104:107], v229, v229 op_sel_hi:[0,0,0]
	v_mfma_scale_f32_16x16x128_f8f6f4 v[108:111], v[154:161], v[196:203], v[108:111], v229, v229 op_sel_hi:[0,0,0]
	v_mfma_scale_f32_16x16x128_f8f6f4 v[112:115], v[146:153], v[232:239], v[112:115], v229, v229 op_sel_hi:[0,0,0]
	v_mfma_scale_f32_16x16x128_f8f6f4 v[116:119], v[154:161], v[232:239], v[116:119], v229, v229 op_sel_hi:[0,0,0]
	v_mfma_scale_f32_16x16x128_f8f6f4 v[120:123], v[146:153], v[240:247], v[120:123], v229, v229 op_sel_hi:[0,0,0]
	v_mfma_scale_f32_16x16x128_f8f6f4 v[124:127], v[154:161], v[240:247], v[124:127], v229, v229 op_sel_hi:[0,0,0]
	s_setprio 0
	s_barrier
	s_add_i32 s42, s42, 2
	s_add_u32 s36, s36, 0x100
	s_addc_u32 s37, s37, 0
	s_cmp_gt_u32 s42, 13
	s_cbranch_scc1 .LBB0_914

.LBB0_914:
	s_min_i32 s7, s74, s65
	s_mul_i32 s7, s7, s44
	s_add_i32 s7, s7, s58
	s_min_i32 s38, s7, 0xffff
	s_lshl_b32 s34, s38, 5
	s_and_b32 s37, s34, 0x7e0
	v_readlane_b32 s34, v254, 13
	v_readlane_b32 s35, v254, 14
	v_mbcnt_lo_u32_b32 v128, -1, 0
	v_mbcnt_hi_u32_b32 v128, -1, v128
	v_readlane_b32 s34, v255, 58
	v_readlane_b32 s35, v255, 59
	s_ashr_i32 s36, s38, 11
	v_and_b32_e32 v129, 0x1ffff8, v128
	v_lshlrev_b32_e32 v128, 2, v128
	v_and_or_b32 v128, v128, 28, s37
	s_ashr_i32 s37, s36, 31
	s_and_b32 s7, s38, 0x7c0
	s_lshl_b64 s[40:41], s[36:37], 24
	v_add_u32_e32 v129, s7, v129
	s_waitcnt lgkmcnt(0)
	s_add_u32 s34, s34, s40
	s_addc_u32 s35, s35, s41
	v_lshl_or_b32 v128, v129, 11, v128
	v_mov_b32_e32 v129, v177
	v_lshl_add_u64 v[152:153], v[128:129], 2, s[34:35]
	v_add_co_u32_e32 v132, vcc, s54, v152
	s_nop 1
	v_addc_co_u32_e32 v133, vcc, 0, v153, vcc
	v_add_co_u32_e32 v136, vcc, s56, v152
	global_load_dwordx4 v[128:131], v[152:153], off nt
	s_nop 0
	global_load_dwordx4 v[132:135], v[132:133], off nt
	v_addc_co_u32_e32 v137, vcc, 0, v153, vcc
	v_add_co_u32_e32 v140, vcc, s57, v152
	s_nop 1
	v_addc_co_u32_e32 v141, vcc, 0, v153, vcc
	v_add_co_u32_e32 v144, vcc, s61, v152
	global_load_dwordx4 v[136:139], v[136:137], off nt
	s_nop 0
	global_load_dwordx4 v[140:143], v[140:141], off nt
	v_addc_co_u32_e32 v145, vcc, 0, v153, vcc
	v_add_co_u32_e32 v148, vcc, 0xa000, v152
	s_nop 1
	v_addc_co_u32_e32 v149, vcc, 0, v153, vcc
	v_add_co_u32_e32 v154, vcc, 0xc000, v152
	global_load_dwordx4 v[144:147], v[144:145], off nt
	s_nop 0
	global_load_dwordx4 v[148:151], v[148:149], off nt
	v_addc_co_u32_e32 v155, vcc, 0, v153, vcc
	v_add_co_u32_e32 v156, vcc, 0xe000, v152
	s_nop 1
	v_addc_co_u32_e32 v157, vcc, 0, v153, vcc
	global_load_dwordx4 v[152:155], v[154:155], off nt
	s_nop 0
	global_load_dwordx4 v[156:159], v[156:157], off nt
	s_and_b64 vcc, exec, s[18:19]
	s_cbranch_vccz .LBB0_916
	s_barrier

.LBB0_1005:
	s_andn2_b64 vcc, exec, s[44:45]
	s_cbranch_vccnz .LBB0_1007
	v_readlane_b32 s40, v255, 60
	v_readlane_b32 s41, v255, 61
	s_ashr_i32 s5, s4, 31
	s_lshl_b64 s[42:43], s[4:5], 13
	s_waitcnt lgkmcnt(0)
	s_add_u32 s5, s40, s42
	s_addc_u32 s27, s41, s43
	s_lshl_b32 s40, s0, 8
	s_ashr_i32 s41, s40, 31
	s_lshl_b64 s[40:41], s[40:41], 2
	s_add_u32 s42, s5, s40
	s_addc_u32 s43, s27, s41

.LBB0_1008:
	s_add_u32 s5, s38, 0x100
	s_addc_u32 s27, s39, 0
	s_lshl_b32 s44, s61, 8
	s_lshl_b32 s29, s61, 19
	s_bitset1_b32 s44, 7
	s_mov_b32 s45, -2
	s_mov_b64 s[38:39], 0
	s_cmp_eq_u32 s45, 12
	s_cselect_b64 s[42:43], -1, 0
	s_and_b64 s[40:41], s[36:37], s[42:43]
	s_andn2_b64 vcc, exec, s[40:41]
	v_mov_b32_e32 v131, v138
	v_mov_b32_e32 v133, v128
	v_add_u32_e32 v135, s58, v142
	s_add_u32 s64, s6, s38
	v_add_u32_e32 v137, s58, v143
	ds_read_b128 v[178:181], v135
	ds_read_b128 v[186:189], v135 offset:2048
	ds_read_b128 v[182:185], v137
	ds_read_b128 v[190:193], v137 offset:2048
	v_add_u32_e32 v135, s59, v142
	s_addc_u32 s65, s7, s39
	v_add_u32_e32 v137, s59, v143
	ds_read_b128 v[194:197], v135
	ds_read_b128 v[202:205], v135 offset:2048
	ds_read_b128 v[198:201], v137
	ds_read_b128 v[206:209], v137 offset:2048
	s_add_u32 s66, s64, 0x5e000100
	s_addc_u32 s67, s65, 0
	s_and_b64 s[40:41], s[42:43], exec
	s_cselect_b32 s41, s11, s67
	s_cselect_b32 s40, s10, s66
	s_add_u32 s66, s5, s38
	s_addc_u32 s67, s27, s39
	s_and_b64 s[42:43], s[42:43], exec
	s_cselect_b32 s43, s35, s67
	s_cselect_b32 s42, s34, s66
	ds_read_b128 v[210:213], v175
	ds_read_b128 v[218:221], v175 offset:2048
	ds_read_b128 v[214:217], v176
	ds_read_b128 v[222:225], v176 offset:2048
	ds_read_b128 v[226:229], v175 offset:4096
	ds_read_b128 v[234:237], v175 offset:6144
	ds_read_b128 v[230:233], v176 offset:4096
	ds_read_b128 v[238:241], v176 offset:6144
	s_add_i32 m0, s1, 0xc000
	v_lshl_add_u64 v[140:141], s[64:65], 0, v[128:129]
	v_lshl_add_u64 v[140:141], v[140:141], 0, s[16:17]
	global_load_lds_dwordx4 v[140:141], off
	v_mov_b32_e32 v139, v129
	v_lshl_add_u64 v[138:139], s[64:65], 0, v[138:139]
	v_lshl_add_u64 v[138:139], v[138:139], 0, s[16:17]
	s_add_i32 m0, s1, 0xe000
	s_nop 0
	global_load_lds_dwordx4 v[138:139], off
	s_waitcnt vmcnt(8)
	s_waitcnt lgkmcnt(0)
	s_barrier
	s_setprio 1
	s_waitcnt lgkmcnt(0)
	v_mfma_scale_f32_16x16x128_f8f6f4 v[100:103], v[178:185], v[210:217], 0, v177, v177 op_sel_hi:[0,0,0]
	v_mfma_scale_f32_16x16x128_f8f6f4 v[96:99], v[186:193], v[210:217], 0, v177, v177 op_sel_hi:[0,0,0]
	v_mfma_scale_f32_16x16x128_f8f6f4 v[92:95], v[178:185], v[218:225], 0, v177, v177 op_sel_hi:[0,0,0]
	v_mfma_scale_f32_16x16x128_f8f6f4 v[88:91], v[186:193], v[218:225], 0, v177, v177 op_sel_hi:[0,0,0]
	v_mfma_scale_f32_16x16x128_f8f6f4 v[84:87], v[178:185], v[226:233], 0, v177, v177 op_sel_hi:[0,0,0]
	v_mfma_scale_f32_16x16x128_f8f6f4 v[80:83], v[186:193], v[226:233], 0, v177, v177 op_sel_hi:[0,0,0]
	v_mfma_scale_f32_16x16x128_f8f6f4 v[242:245], v[178:185], v[234:241], 0, v177, v177 op_sel_hi:[0,0,0]
	v_mfma_scale_f32_16x16x128_f8f6f4 v[246:249], v[186:193], v[234:241], 0, v177, v177 op_sel_hi:[0,0,0]
	s_setprio 0
	s_setprio 1
	v_mfma_scale_f32_16x16x128_f8f6f4 v[40:43], v[194:201], v[234:241], 0, v177, v177 op_sel_hi:[0,0,0]
	v_mfma_scale_f32_16x16x128_f8f6f4 v[32:35], v[202:209], v[234:241], 0, v177, v177 op_sel_hi:[0,0,0]
	v_mfma_scale_f32_16x16x128_f8f6f4 v[250:253], v[194:201], v[210:217], 0, v177, v177 op_sel_hi:[0,0,0]
	v_mfma_scale_f32_16x16x128_f8f6f4 v[144:147], v[202:209], v[210:217], 0, v177, v177 op_sel_hi:[0,0,0]
	v_mfma_scale_f32_16x16x128_f8f6f4 v[148:151], v[194:201], v[218:225], 0, v177, v177 op_sel_hi:[0,0,0]
	v_mfma_scale_f32_16x16x128_f8f6f4 v[152:155], v[202:209], v[218:225], 0, v177, v177 op_sel_hi:[0,0,0]
	v_mfma_scale_f32_16x16x128_f8f6f4 v[156:159], v[194:201], v[226:233], 0, v177, v177 op_sel_hi:[0,0,0]
	v_mfma_scale_f32_16x16x128_f8f6f4 v[160:163], v[202:209], v[226:233], 0, v177, v177 op_sel_hi:[0,0,0]
	s_setprio 0
	s_barrier
	s_add_i32 s64, s58, s48
	s_mov_b32 m0, s64
	s_nop 2
	ds_read_b128 v[48:51], v175 offset:16384
	ds_read_b128 v[56:59], v175 offset:18432
	ds_read_b128 v[52:55], v176 offset:16384
	ds_read_b128 v[60:63], v176 offset:18432
	ds_read_b128 v[64:67], v175 offset:20480
	ds_read_b128 v[72:75], v175 offset:22528
	ds_read_b128 v[68:71], v176 offset:20480
	ds_read_b128 v[76:79], v176 offset:22528
	s_nop 0
	global_load_lds_dwordx4 v136, s[42:43]
	s_add_i32 m0, s64, 0x2000
	s_add_u32 s64, s42, 0x4000
	s_addc_u32 s65, s43, 0
	s_add_i32 s66, s59, s48
	s_nop 0
	global_load_lds_dwordx4 v130, s[42:43]
	s_mov_b32 m0, s66
	s_nop 0
	global_load_lds_dwordx4 v136, s[64:65]
	s_add_i32 m0, s66, 0x2000
	s_nop 0
	global_load_lds_dwordx4 v130, s[64:65]
	s_waitcnt vmcnt(6)
	s_waitcnt lgkmcnt(0)
	s_barrier
	s_setprio 1
	s_waitcnt lgkmcnt(0)
	v_mfma_scale_f32_16x16x128_f8f6f4 v[44:47], v[178:185], v[48:55], 0, v177, v177 op_sel_hi:[0,0,0]
	v_mfma_scale_f32_16x16x128_f8f6f4 v[36:39], v[186:193], v[48:55], 0, v177, v177 op_sel_hi:[0,0,0]
	v_mfma_scale_f32_16x16x128_f8f6f4 v[28:31], v[178:185], v[56:63], 0, v177, v177 op_sel_hi:[0,0,0]
	v_mfma_scale_f32_16x16x128_f8f6f4 v[24:27], v[186:193], v[56:63], 0, v177, v177 op_sel_hi:[0,0,0]
	v_mfma_scale_f32_16x16x128_f8f6f4 v[20:23], v[178:185], v[64:71], 0, v177, v177 op_sel_hi:[0,0,0]
	v_mfma_scale_f32_16x16x128_f8f6f4 v[16:19], v[186:193], v[64:71], 0, v177, v177 op_sel_hi:[0,0,0]
	v_mfma_scale_f32_16x16x128_f8f6f4 v[12:15], v[178:185], v[72:79], 0, v177, v177 op_sel_hi:[0,0,0]
	v_mfma_scale_f32_16x16x128_f8f6f4 v[8:11], v[186:193], v[72:79], 0, v177, v177 op_sel_hi:[0,0,0]
	s_setprio 0
	s_setprio 1
	v_mfma_scale_f32_16x16x128_f8f6f4 v[4:7], v[194:201], v[48:55], 0, v177, v177 op_sel_hi:[0,0,0]
	v_mfma_scale_f32_16x16x128_f8f6f4 v[0:3], v[202:209], v[48:55], 0, v177, v177 op_sel_hi:[0,0,0]
	v_mfma_scale_f32_16x16x128_f8f6f4 v[104:107], v[194:201], v[56:63], 0, v177, v177 op_sel_hi:[0,0,0]
	v_mfma_scale_f32_16x16x128_f8f6f4 v[108:111], v[202:209], v[56:63], 0, v177, v177 op_sel_hi:[0,0,0]
	v_mfma_scale_f32_16x16x128_f8f6f4 v[112:115], v[194:201], v[64:71], 0, v177, v177 op_sel_hi:[0,0,0]
	v_mfma_scale_f32_16x16x128_f8f6f4 v[116:119], v[202:209], v[64:71], 0, v177, v177 op_sel_hi:[0,0,0]
	v_mfma_scale_f32_16x16x128_f8f6f4 v[120:123], v[194:201], v[72:79], 0, v177, v177 op_sel_hi:[0,0,0]
	v_mfma_scale_f32_16x16x128_f8f6f4 v[124:127], v[202:209], v[72:79], 0, v177, v177 op_sel_hi:[0,0,0]
	s_setprio 0
	s_barrier
	s_add_i32 s64, 0, 0x18000
	v_add_u32_e32 v48, s64, v142
	s_add_i32 s65, 0, 0x1c000
	v_add_u32_e32 v49, s64, v143
	ds_read_b128 v[178:181], v48
	ds_read_b128 v[186:189], v48 offset:2048
	ds_read_b128 v[182:185], v49
	ds_read_b128 v[190:193], v49 offset:2048
	v_add_u32_e32 v48, s65, v142
	v_add_u32_e32 v49, s65, v143
	ds_read_b128 v[194:197], v48
	ds_read_b128 v[202:205], v48 offset:2048
	ds_read_b128 v[198:201], v49
	ds_read_b128 v[206:209], v49 offset:2048
	s_mov_b32 m0, s50
	v_mov_b32_e32 v128, v133
	ds_read_b128 v[48:51], v175 offset:32768
	ds_read_b128 v[210:213], v175 offset:34816
	ds_read_b128 v[52:55], v176 offset:32768
	ds_read_b128 v[214:217], v176 offset:34816
	ds_read_b128 v[218:221], v175 offset:36864
	ds_read_b128 v[226:229], v175 offset:38912
	ds_read_b128 v[222:225], v176 offset:36864
	ds_read_b128 v[230:233], v176 offset:38912
	s_mov_b32 m0, s1
	s_nop 0
	global_load_lds_dwordx4 v132, s[40:41]
	s_mov_b32 m0, s49
	s_nop 0
	global_load_lds_dwordx4 v134, s[40:41]
	s_mov_b32 m0, s50
	v_mov_b32_e32 v138, v131
	global_load_lds_dwordx4 v128, s[40:41]
	s_mov_b32 m0, s51
	s_nop 0
	global_load_lds_dwordx4 v138, s[40:41]
	s_waitcnt vmcnt(8)
	s_waitcnt lgkmcnt(0)
	s_barrier
	s_setprio 1
	s_waitcnt lgkmcnt(0)
	v_mfma_scale_f32_16x16x128_f8f6f4 v[100:103], v[178:185], v[48:55], v[100:103], v177, v177 op_sel_hi:[0,0,0]
	v_mfma_scale_f32_16x16x128_f8f6f4 v[96:99], v[186:193], v[48:55], v[96:99], v177, v177 op_sel_hi:[0,0,0]
	v_mfma_scale_f32_16x16x128_f8f6f4 v[92:95], v[178:185], v[210:217], v[92:95], v177, v177 op_sel_hi:[0,0,0]
	v_mfma_scale_f32_16x16x128_f8f6f4 v[88:91], v[186:193], v[210:217], v[88:91], v177, v177 op_sel_hi:[0,0,0]
	v_mfma_scale_f32_16x16x128_f8f6f4 v[84:87], v[178:185], v[218:225], v[84:87], v177, v177 op_sel_hi:[0,0,0]
	v_mfma_scale_f32_16x16x128_f8f6f4 v[80:83], v[186:193], v[218:225], v[80:83], v177, v177 op_sel_hi:[0,0,0]
	v_mfma_scale_f32_16x16x128_f8f6f4 v[76:79], v[178:185], v[226:233], v[242:245], v177, v177 op_sel_hi:[0,0,0]
	v_mfma_scale_f32_16x16x128_f8f6f4 v[72:75], v[186:193], v[226:233], v[246:249], v177, v177 op_sel_hi:[0,0,0]
	s_setprio 0
	s_setprio 1
	v_mfma_scale_f32_16x16x128_f8f6f4 v[68:71], v[194:201], v[48:55], v[250:253], v177, v177 op_sel_hi:[0,0,0]
	v_mfma_scale_f32_16x16x128_f8f6f4 v[64:67], v[202:209], v[48:55], v[144:147], v177, v177 op_sel_hi:[0,0,0]
	v_mfma_scale_f32_16x16x128_f8f6f4 v[60:63], v[194:201], v[210:217], v[148:151], v177, v177 op_sel_hi:[0,0,0]
	v_mfma_scale_f32_16x16x128_f8f6f4 v[56:59], v[202:209], v[210:217], v[152:155], v177, v177 op_sel_hi:[0,0,0]
	v_mfma_scale_f32_16x16x128_f8f6f4 v[52:55], v[194:201], v[218:225], v[156:159], v177, v177 op_sel_hi:[0,0,0]
	v_mfma_scale_f32_16x16x128_f8f6f4 v[48:51], v[202:209], v[218:225], v[160:163], v177, v177 op_sel_hi:[0,0,0]
	v_mfma_scale_f32_16x16x128_f8f6f4 v[40:43], v[194:201], v[226:233], v[40:43], v177, v177 op_sel_hi:[0,0,0]
	v_mfma_scale_f32_16x16x128_f8f6f4 v[32:35], v[202:209], v[226:233], v[32:35], v177, v177 op_sel_hi:[0,0,0]
	s_setprio 0
	s_barrier
	v_mov_b32_e32 v137, v129
	ds_read_b128 v[210:213], v175 offset:49152
	ds_read_b128 v[218:221], v175 offset:51200
	ds_read_b128 v[214:217], v176 offset:49152
	ds_read_b128 v[222:225], v176 offset:51200
	ds_read_b128 v[226:229], v175 offset:53248
	ds_read_b128 v[234:237], v175 offset:55296
	ds_read_b128 v[230:233], v176 offset:53248
	ds_read_b128 v[238:241], v176 offset:55296
	s_add_i32 s64, s64, s48
	v_lshl_add_u64 v[140:141], s[42:43], 0, v[136:137]
	v_lshl_add_u64 v[140:141], v[140:141], 0, s[14:15]
	s_mov_b32 m0, s64
	v_mov_b32_e32 v131, v129
	global_load_lds_dwordx4 v[140:141], off
	s_add_i32 m0, s64, 0x2000
	v_mov_b32_e32 v133, v129
	v_lshl_add_u64 v[140:141], s[42:43], 0, v[130:131]
	s_add_u32 s42, s42, 0x4080
	v_lshl_add_u64 v[140:141], v[140:141], 0, s[14:15]
	s_addc_u32 s43, s43, 0
	s_add_i32 s64, s65, s48
	global_load_lds_dwordx4 v[140:141], off
	s_mov_b32 m0, s64
	v_mov_b32_e32 v135, v129
	global_load_lds_dwordx4 v136, s[42:43]
	s_add_i32 m0, s64, 0x2000
	s_nop 0
	global_load_lds_dwordx4 v130, s[42:43]
	s_mov_b32 m0, s53
	v_lshl_add_u64 v[140:141], s[40:41], 0, v[132:133]
	v_lshl_add_u64 v[140:141], v[140:141], 0, s[14:15]
	global_load_lds_dwordx4 v[140:141], off
	s_mov_b32 m0, s54
	v_lshl_add_u64 v[140:141], s[40:41], 0, v[134:135]
	v_lshl_add_u64 v[140:141], v[140:141], 0, s[14:15]
	global_load_lds_dwordx4 v[140:141], off
	s_waitcnt vmcnt(8)
	s_waitcnt lgkmcnt(0)
	s_barrier
	s_setprio 1
	s_waitcnt lgkmcnt(0)
	v_mfma_scale_f32_16x16x128_f8f6f4 v[44:47], v[178:185], v[210:217], v[44:47], v177, v177 op_sel_hi:[0,0,0]
	v_mfma_scale_f32_16x16x128_f8f6f4 v[36:39], v[186:193], v[210:217], v[36:39], v177, v177 op_sel_hi:[0,0,0]
	v_mfma_scale_f32_16x16x128_f8f6f4 v[28:31], v[178:185], v[218:225], v[28:31], v177, v177 op_sel_hi:[0,0,0]
	v_mfma_scale_f32_16x16x128_f8f6f4 v[24:27], v[186:193], v[218:225], v[24:27], v177, v177 op_sel_hi:[0,0,0]
	v_mfma_scale_f32_16x16x128_f8f6f4 v[20:23], v[178:185], v[226:233], v[20:23], v177, v177 op_sel_hi:[0,0,0]
	v_mfma_scale_f32_16x16x128_f8f6f4 v[16:19], v[186:193], v[226:233], v[16:19], v177, v177 op_sel_hi:[0,0,0]
	v_mfma_scale_f32_16x16x128_f8f6f4 v[12:15], v[178:185], v[234:241], v[12:15], v177, v177 op_sel_hi:[0,0,0]
	v_mfma_scale_f32_16x16x128_f8f6f4 v[8:11], v[186:193], v[234:241], v[8:11], v177, v177 op_sel_hi:[0,0,0]
	s_setprio 0
	s_setprio 1
	v_mfma_scale_f32_16x16x128_f8f6f4 v[4:7], v[194:201], v[210:217], v[4:7], v177, v177 op_sel_hi:[0,0,0]
	v_mfma_scale_f32_16x16x128_f8f6f4 v[0:3], v[202:209], v[210:217], v[0:3], v177, v177 op_sel_hi:[0,0,0]
	v_mfma_scale_f32_16x16x128_f8f6f4 v[104:107], v[194:201], v[218:225], v[104:107], v177, v177 op_sel_hi:[0,0,0]
	v_mfma_scale_f32_16x16x128_f8f6f4 v[108:111], v[202:209], v[218:225], v[108:111], v177, v177 op_sel_hi:[0,0,0]
	v_mfma_scale_f32_16x16x128_f8f6f4 v[112:115], v[194:201], v[226:233], v[112:115], v177, v177 op_sel_hi:[0,0,0]
	v_mfma_scale_f32_16x16x128_f8f6f4 v[116:119], v[202:209], v[226:233], v[116:119], v177, v177 op_sel_hi:[0,0,0]
	v_mfma_scale_f32_16x16x128_f8f6f4 v[120:123], v[194:201], v[234:241], v[120:123], v177, v177 op_sel_hi:[0,0,0]
	v_mfma_scale_f32_16x16x128_f8f6f4 v[124:127], v[202:209], v[234:241], v[124:127], v177, v177 op_sel_hi:[0,0,0]
	s_setprio 0
	s_barrier
	s_add_i32 s45, s45, 2
	s_add_u32 s38, s38, 0x100
	s_addc_u32 s39, s39, 0
	s_branch .LBB0_1010
.LBB0_1009:
	v_add_u32_e32 v135, s58, v142
	s_add_u32 s64, s6, s38
	v_add_u32_e32 v137, s58, v143
	ds_read_b128 v[178:181], v135
	ds_read_b128 v[186:189], v135 offset:2048
	ds_read_b128 v[182:185], v137
	ds_read_b128 v[190:193], v137 offset:2048
	v_add_u32_e32 v135, s59, v142
	s_addc_u32 s65, s7, s39
	v_add_u32_e32 v137, s59, v143
	ds_read_b128 v[194:197], v135
	ds_read_b128 v[202:205], v135 offset:2048
	ds_read_b128 v[198:201], v137
	ds_read_b128 v[206:209], v137 offset:2048
	s_add_u32 s66, s64, 0x5e000100
	s_addc_u32 s67, s65, 0
	s_and_b64 s[40:41], s[42:43], exec
	s_cselect_b32 s41, s11, s67
	s_cselect_b32 s40, s10, s66
	s_add_u32 s66, s5, s38
	s_addc_u32 s67, s27, s39
	s_and_b64 s[42:43], s[42:43], exec
	s_cselect_b32 s43, s35, s67
	s_cselect_b32 s42, s34, s66
	ds_read_b128 v[210:213], v175
	ds_read_b128 v[218:221], v175 offset:2048
	ds_read_b128 v[214:217], v176
	ds_read_b128 v[222:225], v176 offset:2048
	ds_read_b128 v[226:229], v175 offset:4096
	ds_read_b128 v[234:237], v175 offset:6144
	ds_read_b128 v[230:233], v176 offset:4096
	ds_read_b128 v[238:241], v176 offset:6144
	s_add_i32 m0, s1, 0xc000
	v_lshl_add_u64 v[140:141], s[64:65], 0, v[128:129]
	v_lshl_add_u64 v[140:141], v[140:141], 0, s[16:17]
	global_load_lds_dwordx4 v[140:141], off
	v_mov_b32_e32 v139, v129
	v_lshl_add_u64 v[138:139], s[64:65], 0, v[138:139]
	v_lshl_add_u64 v[138:139], v[138:139], 0, s[16:17]
	s_add_i32 m0, s1, 0xe000
	s_nop 0
	global_load_lds_dwordx4 v[138:139], off
	s_waitcnt vmcnt(8)
	s_waitcnt lgkmcnt(0)
	s_barrier
	s_setprio 1
	s_waitcnt lgkmcnt(0)
	v_mfma_scale_f32_16x16x128_f8f6f4 v[100:103], v[178:185], v[210:217], v[100:103], v177, v177 op_sel_hi:[0,0,0]
	v_mfma_scale_f32_16x16x128_f8f6f4 v[96:99], v[186:193], v[210:217], v[96:99], v177, v177 op_sel_hi:[0,0,0]
	v_mfma_scale_f32_16x16x128_f8f6f4 v[92:95], v[178:185], v[218:225], v[92:95], v177, v177 op_sel_hi:[0,0,0]
	v_mfma_scale_f32_16x16x128_f8f6f4 v[88:91], v[186:193], v[218:225], v[88:91], v177, v177 op_sel_hi:[0,0,0]
	v_mfma_scale_f32_16x16x128_f8f6f4 v[84:87], v[178:185], v[226:233], v[84:87], v177, v177 op_sel_hi:[0,0,0]
	v_mfma_scale_f32_16x16x128_f8f6f4 v[80:83], v[186:193], v[226:233], v[80:83], v177, v177 op_sel_hi:[0,0,0]
	v_mfma_scale_f32_16x16x128_f8f6f4 v[242:245], v[178:185], v[234:241], v[76:79], v177, v177 op_sel_hi:[0,0,0]
	v_mfma_scale_f32_16x16x128_f8f6f4 v[246:249], v[186:193], v[234:241], v[72:75], v177, v177 op_sel_hi:[0,0,0]
	s_setprio 0
	s_setprio 1
	v_mfma_scale_f32_16x16x128_f8f6f4 v[40:43], v[194:201], v[234:241], v[40:43], v177, v177 op_sel_hi:[0,0,0]
	v_mfma_scale_f32_16x16x128_f8f6f4 v[32:35], v[202:209], v[234:241], v[32:35], v177, v177 op_sel_hi:[0,0,0]
	v_mfma_scale_f32_16x16x128_f8f6f4 v[250:253], v[194:201], v[210:217], v[68:71], v177, v177 op_sel_hi:[0,0,0]
	v_mfma_scale_f32_16x16x128_f8f6f4 v[144:147], v[202:209], v[210:217], v[64:67], v177, v177 op_sel_hi:[0,0,0]
	v_mfma_scale_f32_16x16x128_f8f6f4 v[148:151], v[194:201], v[218:225], v[60:63], v177, v177 op_sel_hi:[0,0,0]
	v_mfma_scale_f32_16x16x128_f8f6f4 v[152:155], v[202:209], v[218:225], v[56:59], v177, v177 op_sel_hi:[0,0,0]
	v_mfma_scale_f32_16x16x128_f8f6f4 v[156:159], v[194:201], v[226:233], v[52:55], v177, v177 op_sel_hi:[0,0,0]
	v_mfma_scale_f32_16x16x128_f8f6f4 v[160:163], v[202:209], v[226:233], v[48:51], v177, v177 op_sel_hi:[0,0,0]
	s_setprio 0
	s_barrier
	s_add_i32 s64, s58, s48
	s_mov_b32 m0, s64
	s_nop 2
	ds_read_b128 v[48:51], v175 offset:16384
	ds_read_b128 v[56:59], v175 offset:18432
	ds_read_b128 v[52:55], v176 offset:16384
	ds_read_b128 v[60:63], v176 offset:18432
	ds_read_b128 v[64:67], v175 offset:20480
	ds_read_b128 v[72:75], v175 offset:22528
	ds_read_b128 v[68:71], v176 offset:20480
	ds_read_b128 v[76:79], v176 offset:22528
	s_nop 0
	global_load_lds_dwordx4 v136, s[42:43]
	s_add_i32 m0, s64, 0x2000
	s_add_u32 s64, s42, 0x4000
	s_addc_u32 s65, s43, 0
	s_add_i32 s66, s59, s48
	s_nop 0
	global_load_lds_dwordx4 v130, s[42:43]
	s_mov_b32 m0, s66
	s_nop 0
	global_load_lds_dwordx4 v136, s[64:65]
	s_add_i32 m0, s66, 0x2000
	s_nop 0
	global_load_lds_dwordx4 v130, s[64:65]
	s_waitcnt vmcnt(6)
	s_waitcnt lgkmcnt(0)
	s_barrier
	s_setprio 1
	s_waitcnt lgkmcnt(0)
	v_mfma_scale_f32_16x16x128_f8f6f4 v[44:47], v[178:185], v[48:55], v[44:47], v177, v177 op_sel_hi:[0,0,0]
	v_mfma_scale_f32_16x16x128_f8f6f4 v[36:39], v[186:193], v[48:55], v[36:39], v177, v177 op_sel_hi:[0,0,0]
	v_mfma_scale_f32_16x16x128_f8f6f4 v[28:31], v[178:185], v[56:63], v[28:31], v177, v177 op_sel_hi:[0,0,0]
	v_mfma_scale_f32_16x16x128_f8f6f4 v[24:27], v[186:193], v[56:63], v[24:27], v177, v177 op_sel_hi:[0,0,0]
	v_mfma_scale_f32_16x16x128_f8f6f4 v[20:23], v[178:185], v[64:71], v[20:23], v177, v177 op_sel_hi:[0,0,0]
	v_mfma_scale_f32_16x16x128_f8f6f4 v[16:19], v[186:193], v[64:71], v[16:19], v177, v177 op_sel_hi:[0,0,0]
	v_mfma_scale_f32_16x16x128_f8f6f4 v[12:15], v[178:185], v[72:79], v[12:15], v177, v177 op_sel_hi:[0,0,0]
	v_mfma_scale_f32_16x16x128_f8f6f4 v[8:11], v[186:193], v[72:79], v[8:11], v177, v177 op_sel_hi:[0,0,0]
	s_setprio 0
	s_setprio 1
	v_mfma_scale_f32_16x16x128_f8f6f4 v[4:7], v[194:201], v[48:55], v[4:7], v177, v177 op_sel_hi:[0,0,0]
	v_mfma_scale_f32_16x16x128_f8f6f4 v[0:3], v[202:209], v[48:55], v[0:3], v177, v177 op_sel_hi:[0,0,0]
	v_mfma_scale_f32_16x16x128_f8f6f4 v[104:107], v[194:201], v[56:63], v[104:107], v177, v177 op_sel_hi:[0,0,0]
	v_mfma_scale_f32_16x16x128_f8f6f4 v[108:111], v[202:209], v[56:63], v[108:111], v177, v177 op_sel_hi:[0,0,0]
	v_mfma_scale_f32_16x16x128_f8f6f4 v[112:115], v[194:201], v[64:71], v[112:115], v177, v177 op_sel_hi:[0,0,0]
	v_mfma_scale_f32_16x16x128_f8f6f4 v[116:119], v[202:209], v[64:71], v[116:119], v177, v177 op_sel_hi:[0,0,0]
	v_mfma_scale_f32_16x16x128_f8f6f4 v[120:123], v[194:201], v[72:79], v[120:123], v177, v177 op_sel_hi:[0,0,0]
	v_mfma_scale_f32_16x16x128_f8f6f4 v[124:127], v[202:209], v[72:79], v[124:127], v177, v177 op_sel_hi:[0,0,0]
	s_setprio 0
	s_barrier
	s_add_i32 s64, 0, 0x18000
	v_add_u32_e32 v48, s64, v142
	s_add_i32 s65, 0, 0x1c000
	v_add_u32_e32 v49, s64, v143
	ds_read_b128 v[178:181], v48
	ds_read_b128 v[186:189], v48 offset:2048
	ds_read_b128 v[182:185], v49
	ds_read_b128 v[190:193], v49 offset:2048
	v_add_u32_e32 v48, s65, v142
	v_add_u32_e32 v49, s65, v143
	ds_read_b128 v[194:197], v48
	ds_read_b128 v[202:205], v48 offset:2048
	ds_read_b128 v[198:201], v49
	ds_read_b128 v[206:209], v49 offset:2048
	s_mov_b32 m0, s50
	v_mov_b32_e32 v128, v133
	ds_read_b128 v[48:51], v175 offset:32768
	ds_read_b128 v[210:213], v175 offset:34816
	ds_read_b128 v[52:55], v176 offset:32768
	ds_read_b128 v[214:217], v176 offset:34816
	ds_read_b128 v[218:221], v175 offset:36864
	ds_read_b128 v[226:229], v175 offset:38912
	ds_read_b128 v[222:225], v176 offset:36864
	ds_read_b128 v[230:233], v176 offset:38912
	s_mov_b32 m0, s1
	s_nop 0
	global_load_lds_dwordx4 v132, s[40:41]
	s_mov_b32 m0, s49
	s_nop 0
	global_load_lds_dwordx4 v134, s[40:41]
	s_mov_b32 m0, s50
	v_mov_b32_e32 v138, v131
	global_load_lds_dwordx4 v128, s[40:41]
	s_mov_b32 m0, s51
	s_nop 0
	global_load_lds_dwordx4 v138, s[40:41]
	s_waitcnt vmcnt(8)
	s_waitcnt lgkmcnt(0)
	s_barrier
	s_setprio 1
	s_waitcnt lgkmcnt(0)
	v_mfma_scale_f32_16x16x128_f8f6f4 v[100:103], v[178:185], v[48:55], v[100:103], v177, v177 op_sel_hi:[0,0,0]
	v_mfma_scale_f32_16x16x128_f8f6f4 v[96:99], v[186:193], v[48:55], v[96:99], v177, v177 op_sel_hi:[0,0,0]
	v_mfma_scale_f32_16x16x128_f8f6f4 v[92:95], v[178:185], v[210:217], v[92:95], v177, v177 op_sel_hi:[0,0,0]
	v_mfma_scale_f32_16x16x128_f8f6f4 v[88:91], v[186:193], v[210:217], v[88:91], v177, v177 op_sel_hi:[0,0,0]
	v_mfma_scale_f32_16x16x128_f8f6f4 v[84:87], v[178:185], v[218:225], v[84:87], v177, v177 op_sel_hi:[0,0,0]
	v_mfma_scale_f32_16x16x128_f8f6f4 v[80:83], v[186:193], v[218:225], v[80:83], v177, v177 op_sel_hi:[0,0,0]
	v_mfma_scale_f32_16x16x128_f8f6f4 v[76:79], v[178:185], v[226:233], v[242:245], v177, v177 op_sel_hi:[0,0,0]
	v_mfma_scale_f32_16x16x128_f8f6f4 v[72:75], v[186:193], v[226:233], v[246:249], v177, v177 op_sel_hi:[0,0,0]
	s_setprio 0
	s_setprio 1
	v_mfma_scale_f32_16x16x128_f8f6f4 v[68:71], v[194:201], v[48:55], v[250:253], v177, v177 op_sel_hi:[0,0,0]
	v_mfma_scale_f32_16x16x128_f8f6f4 v[64:67], v[202:209], v[48:55], v[144:147], v177, v177 op_sel_hi:[0,0,0]
	v_mfma_scale_f32_16x16x128_f8f6f4 v[60:63], v[194:201], v[210:217], v[148:151], v177, v177 op_sel_hi:[0,0,0]
	v_mfma_scale_f32_16x16x128_f8f6f4 v[56:59], v[202:209], v[210:217], v[152:155], v177, v177 op_sel_hi:[0,0,0]
	v_mfma_scale_f32_16x16x128_f8f6f4 v[52:55], v[194:201], v[218:225], v[156:159], v177, v177 op_sel_hi:[0,0,0]
	v_mfma_scale_f32_16x16x128_f8f6f4 v[48:51], v[202:209], v[218:225], v[160:163], v177, v177 op_sel_hi:[0,0,0]
	v_mfma_scale_f32_16x16x128_f8f6f4 v[40:43], v[194:201], v[226:233], v[40:43], v177, v177 op_sel_hi:[0,0,0]
	v_mfma_scale_f32_16x16x128_f8f6f4 v[32:35], v[202:209], v[226:233], v[32:35], v177, v177 op_sel_hi:[0,0,0]
	s_setprio 0
	s_barrier
	v_mov_b32_e32 v137, v129
	ds_read_b128 v[210:213], v175 offset:49152
	ds_read_b128 v[218:221], v175 offset:51200
	ds_read_b128 v[214:217], v176 offset:49152
	ds_read_b128 v[222:225], v176 offset:51200
	ds_read_b128 v[226:229], v175 offset:53248
	ds_read_b128 v[234:237], v175 offset:55296
	ds_read_b128 v[230:233], v176 offset:53248
	ds_read_b128 v[238:241], v176 offset:55296
	s_add_i32 s64, s64, s48
	v_lshl_add_u64 v[140:141], s[42:43], 0, v[136:137]
	v_lshl_add_u64 v[140:141], v[140:141], 0, s[14:15]
	s_mov_b32 m0, s64
	v_mov_b32_e32 v131, v129
	global_load_lds_dwordx4 v[140:141], off
	s_add_i32 m0, s64, 0x2000
	v_mov_b32_e32 v133, v129
	v_lshl_add_u64 v[140:141], s[42:43], 0, v[130:131]
	s_add_u32 s42, s42, 0x4080
	v_lshl_add_u64 v[140:141], v[140:141], 0, s[14:15]
	s_addc_u32 s43, s43, 0
	s_add_i32 s64, s65, s48
	global_load_lds_dwordx4 v[140:141], off
	s_mov_b32 m0, s64
	v_mov_b32_e32 v135, v129
	global_load_lds_dwordx4 v136, s[42:43]
	s_add_i32 m0, s64, 0x2000
	s_nop 0
	global_load_lds_dwordx4 v130, s[42:43]
	s_mov_b32 m0, s53
	v_lshl_add_u64 v[140:141], s[40:41], 0, v[132:133]
	v_lshl_add_u64 v[140:141], v[140:141], 0, s[14:15]
	global_load_lds_dwordx4 v[140:141], off
	s_mov_b32 m0, s54
	v_lshl_add_u64 v[140:141], s[40:41], 0, v[134:135]
	v_lshl_add_u64 v[140:141], v[140:141], 0, s[14:15]
	global_load_lds_dwordx4 v[140:141], off
	s_waitcnt vmcnt(8)
	s_waitcnt lgkmcnt(0)
	s_barrier
	s_setprio 1
	s_waitcnt lgkmcnt(0)
	v_mfma_scale_f32_16x16x128_f8f6f4 v[44:47], v[178:185], v[210:217], v[44:47], v177, v177 op_sel_hi:[0,0,0]
	v_mfma_scale_f32_16x16x128_f8f6f4 v[36:39], v[186:193], v[210:217], v[36:39], v177, v177 op_sel_hi:[0,0,0]
	v_mfma_scale_f32_16x16x128_f8f6f4 v[28:31], v[178:185], v[218:225], v[28:31], v177, v177 op_sel_hi:[0,0,0]
	v_mfma_scale_f32_16x16x128_f8f6f4 v[24:27], v[186:193], v[218:225], v[24:27], v177, v177 op_sel_hi:[0,0,0]
	v_mfma_scale_f32_16x16x128_f8f6f4 v[20:23], v[178:185], v[226:233], v[20:23], v177, v177 op_sel_hi:[0,0,0]
	v_mfma_scale_f32_16x16x128_f8f6f4 v[16:19], v[186:193], v[226:233], v[16:19], v177, v177 op_sel_hi:[0,0,0]
	v_mfma_scale_f32_16x16x128_f8f6f4 v[12:15], v[178:185], v[234:241], v[12:15], v177, v177 op_sel_hi:[0,0,0]
	v_mfma_scale_f32_16x16x128_f8f6f4 v[8:11], v[186:193], v[234:241], v[8:11], v177, v177 op_sel_hi:[0,0,0]
	s_setprio 0
	s_setprio 1
	v_mfma_scale_f32_16x16x128_f8f6f4 v[4:7], v[194:201], v[210:217], v[4:7], v177, v177 op_sel_hi:[0,0,0]
	v_mfma_scale_f32_16x16x128_f8f6f4 v[0:3], v[202:209], v[210:217], v[0:3], v177, v177 op_sel_hi:[0,0,0]
	v_mfma_scale_f32_16x16x128_f8f6f4 v[104:107], v[194:201], v[218:225], v[104:107], v177, v177 op_sel_hi:[0,0,0]
	v_mfma_scale_f32_16x16x128_f8f6f4 v[108:111], v[202:209], v[218:225], v[108:111], v177, v177 op_sel_hi:[0,0,0]
	v_mfma_scale_f32_16x16x128_f8f6f4 v[112:115], v[194:201], v[226:233], v[112:115], v177, v177 op_sel_hi:[0,0,0]
	v_mfma_scale_f32_16x16x128_f8f6f4 v[116:119], v[202:209], v[226:233], v[116:119], v177, v177 op_sel_hi:[0,0,0]
	v_mfma_scale_f32_16x16x128_f8f6f4 v[120:123], v[194:201], v[234:241], v[120:123], v177, v177 op_sel_hi:[0,0,0]
	v_mfma_scale_f32_16x16x128_f8f6f4 v[124:127], v[202:209], v[234:241], v[124:127], v177, v177 op_sel_hi:[0,0,0]
	s_setprio 0
	s_barrier
	s_add_i32 s45, s45, 2
	s_add_u32 s38, s38, 0x100
	s_addc_u32 s39, s39, 0
	s_cmp_gt_u32 s45, 13
	s_cbranch_scc1 .LBB0_1012
